# attention softmax row-sum: adjacent scalar f32 adds on aligned register pairs fused into v_pk_add_f32 (38 pairs)
# speedup vs baseline: 1.0073x; 1.0013x over previous
.LBB0_237:
	v_and_b32_e32 v163, 63, v39
	v_lshlrev_b32_e32 v40, 4, v163
	v_lshlrev_b32_e32 v39, 3, v163
	v_and_b32_e32 v40, 0xc0, v40
	v_lshlrev_b32_e32 v41, 1, v163
	s_cmp_lg_u32 0, -1
	v_and_or_b32 v40, v39, 24, v40
	v_and_b32_e32 v41, 32, v41
	v_and_b32_e32 v39, 0x100, v39
	s_cselect_b32 s4, 0, 0
	v_or3_b32 v39, v40, v41, v39
	v_add_u32_e32 v166, s4, v39
	v_max_f32_e32 v39, v18, v19
	v_max3_f32 v39, v39, v20, v21
	v_max3_f32 v39, v39, v22, v23
	v_max3_f32 v39, v39, v24, v25
	v_max3_f32 v39, v39, v26, v27
	v_max3_f32 v39, v39, v28, v29
	v_max3_f32 v39, v39, v30, v31
	v_max3_f32 v39, v39, v32, v33
	v_max3_f32 v39, v39, v2, v3
	v_max3_f32 v39, v39, v4, v5
	v_max3_f32 v39, v39, v6, v7
	v_max3_f32 v39, v39, v8, v9
	v_max3_f32 v39, v39, v10, v11
	v_max3_f32 v39, v39, v12, v13
	v_max3_f32 v39, v39, v14, v15
	v_max3_f32 v39, v39, v16, v17
	v_mov_b32_e32 v40, v39
	s_nop 1
	v_permlane32_swap_b32_e32 v39, v40
	v_max_f32_e32 v39, v39, v40
	v_add_f32_e32 v40, 0x7149f2ca, v39
	s_add_i32 s83, s4, s86
	v_mul_f32_e32 v40, 0x3e000000, v40
	s_add_i32 s85, s83, 0x10000
	v_cmp_ge_f32_e32 vcc, s33, v40
	s_cmp_eq_u64 vcc, exec
	v_max_f32_e32 v39, 0xf149f2ca, v39
	v_sub_f32_e32 v40, 0xf149f2ca, v39
	s_cselect_b64 s[4:5], -1, 0
	v_mul_f32_e32 v40, 0x3e38aa3b, v40
	v_cndmask_b32_e64 v116, v39, v161, s[4:5]
	v_exp_f32_e32 v179, v40
	v_mul_f32_e32 v40, 0xbe38aa3b, v116
	v_pk_fma_f32 v[32:33], v[32:33], s[84:85], v[40:41] op_sel_hi:[1,0,0]
	v_pk_fma_f32 v[30:31], v[30:31], s[84:85], v[40:41] op_sel_hi:[1,0,0]
	v_pk_fma_f32 v[28:29], v[28:29], s[84:85], v[40:41] op_sel_hi:[1,0,0]
	v_pk_fma_f32 v[26:27], v[26:27], s[84:85], v[40:41] op_sel_hi:[1,0,0]
	v_pk_fma_f32 v[24:25], v[24:25], s[84:85], v[40:41] op_sel_hi:[1,0,0]
	v_pk_fma_f32 v[22:23], v[22:23], s[84:85], v[40:41] op_sel_hi:[1,0,0]
	v_pk_fma_f32 v[20:21], v[20:21], s[84:85], v[40:41] op_sel_hi:[1,0,0]
	v_pk_fma_f32 v[18:19], v[18:19], s[84:85], v[40:41] op_sel_hi:[1,0,0]
	v_exp_f32_e32 v58, v20
	v_exp_f32_e32 v56, v18
	v_exp_f32_e32 v57, v19
	v_exp_f32_e32 v59, v21
	v_exp_f32_e32 v60, v22
	v_exp_f32_e32 v61, v23
	v_exp_f32_e32 v62, v24
	v_exp_f32_e32 v63, v25
	v_exp_f32_e32 v26, v26
	v_exp_f32_e32 v27, v27
	v_exp_f32_e32 v28, v28
	v_exp_f32_e32 v29, v29
	v_exp_f32_e32 v30, v30
	v_exp_f32_e32 v31, v31
	v_exp_f32_e32 v32, v32
	v_exp_f32_e32 v33, v33
	s_waitcnt vmcnt(0)
	v_pk_fma_f32 v[42:43], v[16:17], s[84:85], v[40:41] op_sel_hi:[1,0,0]
	v_pk_fma_f32 v[44:45], v[14:15], s[84:85], v[40:41] op_sel_hi:[1,0,0]
	v_pk_fma_f32 v[46:47], v[12:13], s[84:85], v[40:41] op_sel_hi:[1,0,0]
	v_pk_fma_f32 v[48:49], v[10:11], s[84:85], v[40:41] op_sel_hi:[1,0,0]
	v_pk_fma_f32 v[50:51], v[8:9], s[84:85], v[40:41] op_sel_hi:[1,0,0]
	v_pk_fma_f32 v[52:53], v[6:7], s[84:85], v[40:41] op_sel_hi:[1,0,0]
	v_pk_fma_f32 v[54:55], v[4:5], s[84:85], v[40:41] op_sel_hi:[1,0,0]
	v_pk_fma_f32 v[40:41], v[2:3], s[84:85], v[40:41] op_sel_hi:[1,0,0]
	s_barrier
	s_add_u32 s6, s90, 0x80000
	s_addc_u32 s7, s91, 0
	s_mov_b32 m0, s85
	s_nop 0
	global_load_lds_dwordx4 v168, s[6:7] offset:0
	s_add_u32 s6, s92, 0x80000
	s_addc_u32 s7, s93, 0
	s_add_i32 s82, s83, 0x8000
	s_mov_b32 m0, s82
	s_nop 0
	global_load_lds_dwordx4 v169, s[6:7] offset:0
	s_add_i32 s83, s83, 0xa000
	s_mov_b32 m0, s83
	s_nop 0
	global_load_lds_dwordx4 v170, s[6:7] offset:0
	s_add_i32 s6, 0, 0x12000
	v_add_u32_e32 v10, s6, v35
	v_add_u32_e32 v175, v10, v37
	ds_read_b128 v[2:5], v175
	ds_read_b128 v[6:9], v175 offset:4096
	v_add_u32_e32 v176, v10, v38
	v_add_u32_e32 v177, v10, v36
	v_add_u32_e32 v178, v10, v34
	s_waitcnt lgkmcnt(1)
	v_mfma_f32_32x32x16_bf16 v[66:81], v[2:5], v[110:113], 0
	ds_read_b128 v[2:5], v176
	ds_read_b128 v[10:13], v176 offset:4096
	ds_read_b128 v[14:17], v177
	ds_read_b128 v[18:21], v177 offset:4096
	v_exp_f32_e32 v34, v40
	v_exp_f32_e32 v35, v41
	v_exp_f32_e32 v36, v54
	v_exp_f32_e32 v37, v55
	v_exp_f32_e32 v38, v52
	v_exp_f32_e32 v39, v53
	s_waitcnt lgkmcnt(4)
	v_mfma_f32_32x32x16_bf16 v[82:97], v[6:9], v[110:113], 0
	ds_read_b128 v[6:9], v178
	ds_read_b128 v[22:25], v178 offset:4096
	v_exp_f32_e32 v40, v50
	v_exp_f32_e32 v41, v51
	v_exp_f32_e32 v48, v48
	v_exp_f32_e32 v49, v49
	v_exp_f32_e32 v46, v46
	v_exp_f32_e32 v47, v47
	s_waitcnt lgkmcnt(5)
	v_mfma_f32_32x32x16_bf16 v[66:81], v[2:5], v[106:109], v[66:81]
	v_pk_add_f32 v[4:5], v[58:59], v[36:37]
	v_pk_add_f32 v[52:53], v[60:61], v[38:39]
	v_pk_add_f32 v[2:3], v[28:29], v[46:47]
	v_pk_add_f32 v[2:3], v[4:5], v[2:3]
	s_waitcnt lgkmcnt(4)
	v_mfma_f32_32x32x16_bf16 v[82:97], v[10:13], v[106:109], v[82:97]
	v_exp_f32_e32 v10, v44
	v_exp_f32_e32 v12, v42
	v_exp_f32_e32 v13, v43
	v_exp_f32_e32 v11, v45
	v_pk_add_f32 v[44:45], v[56:57], v[34:35]
	v_pk_add_f32 v[42:43], v[32:33], v[12:13]
	s_waitcnt lgkmcnt(3)
	v_mfma_f32_32x32x16_bf16 v[66:81], v[14:17], v[102:105], v[66:81]
	v_pk_add_f32 v[14:15], v[62:63], v[40:41]
	v_pk_add_f32 v[16:17], v[26:27], v[48:49]
	v_pk_add_f32 v[50:51], v[30:31], v[10:11]
	v_pk_add_f32 v[16:17], v[44:45], v[16:17]
	v_pk_add_f32 v[50:51], v[52:53], v[50:51]
	v_pk_add_f32 v[14:15], v[14:15], v[42:43]
	v_pk_add_f32 v[4:5], v[16:17], v[50:51]
	s_waitcnt lgkmcnt(2)
	v_mfma_f32_32x32x16_bf16 v[82:97], v[18:21], v[102:105], v[82:97]
	v_pk_add_f32 v[2:3], v[2:3], v[14:15]
	v_pk_add_f32 v[2:3], v[4:5], v[2:3]
	v_add_f32_e64 v114, v2, v3
	v_add_f32_e64 v115, v3, v2
	v_cvt_pk_bf16_f32 v2, v56, v57
	v_cvt_pk_bf16_f32 v3, v58, v59
	s_waitcnt lgkmcnt(1)
	v_mfma_f32_32x32x16_bf16 v[66:81], v[6:9], v[98:101], v[66:81]
	v_mov_b32_e32 v115, v114
	v_cvt_pk_bf16_f32 v4, v60, v61
	v_cvt_pk_bf16_f32 v5, v62, v63
	s_nop 1
	v_permlane32_swap_b32_e32 v114, v115
	v_permlane32_swap_b32_e32 v2, v4
	s_waitcnt lgkmcnt(0)
	v_mfma_f32_32x32x16_bf16 v[82:97], v[22:25], v[98:101], v[82:97]
	v_permlane32_swap_b32_e32 v3, v5
	v_cvt_pk_bf16_f32 v120, v26, v27
	v_cvt_pk_bf16_f32 v121, v28, v29
	v_cvt_pk_bf16_f32 v122, v30, v31
	v_cvt_pk_bf16_f32 v123, v32, v33
	v_cvt_pk_bf16_f32 v124, v34, v35
	v_cvt_pk_bf16_f32 v125, v36, v37
	v_cvt_pk_bf16_f32 v126, v38, v39
	v_cvt_pk_bf16_f32 v127, v40, v41
	v_cvt_pk_bf16_f32 v128, v48, v49
	v_cvt_pk_bf16_f32 v129, v46, v47
	v_cvt_pk_bf16_f32 v130, v10, v11
	v_cvt_pk_bf16_f32 v131, v12, v13
	s_nop 0
	v_permlane32_swap_b32_e32 v120, v122
	v_permlane32_swap_b32_e32 v121, v123
	v_permlane32_swap_b32_e32 v124, v126
	v_permlane32_swap_b32_e32 v125, v127
	v_permlane32_swap_b32_e32 v128, v130
	v_permlane32_swap_b32_e32 v129, v131
	ds_read_b64_tr_b16 v[6:7], v166 offset:0
	ds_read_b64_tr_b16 v[8:9], v166 offset:0x800
	ds_read_b64_tr_b16 v[10:11], v166 offset:0x1000
	ds_read_b64_tr_b16 v[12:13], v166 offset:0x1800
	ds_read_b64_tr_b16 v[14:15], v166 offset:0x2000
	ds_read_b64_tr_b16 v[16:17], v166 offset:0x2800
	ds_read_b64_tr_b16 v[34:35], v166 offset:0x3000
	ds_read_b64_tr_b16 v[36:37], v166 offset:0x3800
	ds_read_b64_tr_b16 v[38:39], v166 offset:0x200
	ds_read_b64_tr_b16 v[40:41], v166 offset:0xa00
	ds_read_b64_tr_b16 v[50:51], v166 offset:0x1200
	ds_read_b64_tr_b16 v[52:53], v166 offset:0x1a00
	ds_read_b64_tr_b16 v[54:55], v166 offset:0x2200
	ds_read_b64_tr_b16 v[56:57], v166 offset:0x2a00
	ds_read_b64_tr_b16 v[58:59], v166 offset:0x3200
	ds_read_b64_tr_b16 v[60:61], v166 offset:0x3a00
	s_waitcnt lgkmcnt(8)
	s_nop 0
	v_mfma_f32_32x32x16_bf16 v[18:33], v[2:5], v[6:9], 0
	v_mfma_f32_32x32x16_bf16 v[18:33], v[120:123], v[10:13], v[18:33]
	v_mfma_f32_32x32x16_bf16 v[18:33], v[124:127], v[14:17], v[18:33]
	v_mfma_f32_32x32x16_bf16 v[18:33], v[128:131], v[34:37], v[18:33]
	ds_read_b64_tr_b16 v[6:7], v166 offset:0x400
	ds_read_b64_tr_b16 v[8:9], v166 offset:0xc00
	ds_read_b64_tr_b16 v[10:11], v166 offset:0x1400
	ds_read_b64_tr_b16 v[12:13], v166 offset:0x1c00
	ds_read_b64_tr_b16 v[14:15], v166 offset:0x2400
	ds_read_b64_tr_b16 v[16:17], v166 offset:0x2c00
	ds_read_b64_tr_b16 v[132:133], v166 offset:0x3400
	ds_read_b64_tr_b16 v[134:135], v166 offset:0x3c00
	s_waitcnt lgkmcnt(8)
	v_mfma_f32_32x32x16_bf16 v[34:49], v[2:5], v[38:41], 0
	v_mfma_f32_32x32x16_bf16 v[34:49], v[120:123], v[50:53], v[34:49]
	v_mfma_f32_32x32x16_bf16 v[34:49], v[124:127], v[54:57], v[34:49]
	v_mfma_f32_32x32x16_bf16 v[34:49], v[128:131], v[58:61], v[34:49]
	ds_read_b64_tr_b16 v[140:141], v166 offset:0x600
	ds_read_b64_tr_b16 v[142:143], v166 offset:0xe00
	ds_read_b64_tr_b16 v[144:145], v166 offset:0x1600
	ds_read_b64_tr_b16 v[146:147], v166 offset:0x1e00
	ds_read_b64_tr_b16 v[148:149], v166 offset:0x2600
	ds_read_b64_tr_b16 v[150:151], v166 offset:0x2e00
	ds_read_b64_tr_b16 v[152:153], v166 offset:0x3600
	ds_read_b64_tr_b16 v[154:155], v166 offset:0x3e00
	s_waitcnt lgkmcnt(8)
	v_mfma_f32_32x32x16_bf16 v[50:65], v[2:5], v[6:9], 0
	v_mfma_f32_32x32x16_bf16 v[50:65], v[120:123], v[10:13], v[50:65]
	v_mfma_f32_32x32x16_bf16 v[50:65], v[124:127], v[14:17], v[50:65]
	v_mfma_f32_32x32x16_bf16 v[50:65], v[128:131], v[132:135], v[50:65]
	s_waitcnt lgkmcnt(0)
	v_mfma_f32_32x32x16_bf16 v[2:17], v[2:5], v[140:143], 0
	s_cmpk_gt_i32 s77, 0x7e
	v_mfma_f32_32x32x16_bf16 v[2:17], v[120:123], v[144:147], v[2:17]
	v_mfma_f32_32x32x16_bf16 v[2:17], v[124:127], v[148:151], v[2:17]
	v_mfma_f32_32x32x16_bf16 v[2:17], v[128:131], v[152:155], v[2:17]
	s_cbranch_scc1 .LBB0_239
	s_movk_i32 s60, 0x5a
	s_movk_i32 s62, 0x5b
	v_cmp_gt_i32_e64 s[60:61], s60, v167
	v_cmp_gt_i32_e64 s[62:63], s62, v167
	s_and_b64 s[60:61], s[62:63], s[60:61]
	s_movk_i32 s28, 0x58
	v_cndmask_b32_e64 v81, v81, v160, s[62:63]
	s_movk_i32 s62, 0x59
	v_cmp_gt_i32_e64 s[62:63], s62, v167
	s_movk_i32 s26, 0x53
	v_cmp_gt_i32_e64 s[58:59], s28, v167
	v_cndmask_b32_e64 v80, v80, v160, s[60:61]
	s_and_b64 s[60:61], s[60:61], s[62:63]
	s_movk_i32 s24, 0x52
	v_cmp_gt_i32_e64 s[56:57], s26, v167
	s_and_b64 s[58:59], s[60:61], s[58:59]
	s_movk_i32 s22, 0x51
	v_cmp_gt_i32_e64 s[54:55], s24, v167
	s_and_b64 s[56:57], s[58:59], s[56:57]
	s_movk_i32 s20, 0x50
	v_cmp_gt_i32_e64 s[52:53], s22, v167
	s_and_b64 s[54:55], s[56:57], s[54:55]
	s_movk_i32 s18, 0x4b
	v_cmp_gt_i32_e64 s[50:51], s20, v167
	s_and_b64 s[52:53], s[54:55], s[52:53]
	s_movk_i32 s16, 0x4a
	v_cmp_gt_i32_e64 s[48:49], s18, v167
	s_and_b64 s[50:51], s[52:53], s[50:51]
	s_movk_i32 s14, 0x49
	v_cmp_gt_i32_e64 s[44:45], s16, v167
	s_and_b64 s[48:49], s[50:51], s[48:49]
	s_movk_i32 s12, 0x48
	v_cmp_gt_i32_e64 s[42:43], s14, v167
	s_and_b64 s[44:45], s[48:49], s[44:45]
	s_movk_i32 s10, 0x43
	v_cmp_gt_i32_e64 s[40:41], s12, v167
	s_and_b64 s[42:43], s[44:45], s[42:43]
	s_movk_i32 s6, 0x60
	s_movk_i32 s8, 0x42
	v_cmp_gt_i32_e64 s[38:39], s10, v167
	s_and_b64 s[40:41], s[42:43], s[40:41]
	v_cmp_gt_i32_e32 vcc, s6, v167
	s_movk_i32 s6, 0x41
	v_cmp_gt_i32_e64 s[36:37], s8, v167
	s_and_b64 s[38:39], s[40:41], s[38:39]
	v_cmp_gt_i32_e64 s[34:35], s6, v167
	s_and_b64 s[36:37], s[38:39], s[36:37]
	v_cmp_gt_i32_e64 s[30:31], 64, v167
	s_and_b64 s[34:35], s[36:37], s[34:35]
	s_and_b64 s[30:31], s[34:35], s[30:31]
	v_cndmask_b32_e64 v79, v79, v160, s[60:61]
	s_movk_i32 s60, 0x7a
	v_cndmask_b32_e64 v66, v66, v160, s[30:31]
	s_movk_i32 s30, 0x7b
	s_movk_i32 s62, 0x79
	v_cmp_gt_i32_e64 s[60:61], s60, v167
	v_cmp_gt_i32_e64 s[30:31], s30, v167
	s_movk_i32 s28, 0x78
	v_cmp_gt_i32_e64 s[62:63], s62, v167
	v_cndmask_b32_e64 v97, v97, v160, s[30:31]
	s_and_b64 s[30:31], s[30:31], s[60:61]
	s_movk_i32 s26, 0x73
	v_cmp_gt_i32_e64 s[28:29], s28, v167
	v_cndmask_b32_e64 v96, v96, v160, s[30:31]
	s_and_b64 s[30:31], s[30:31], s[62:63]
	s_movk_i32 s24, 0x72
	v_cmp_gt_i32_e64 s[26:27], s26, v167
	s_and_b64 s[28:29], s[30:31], s[28:29]
	s_movk_i32 s22, 0x71
	v_cmp_gt_i32_e64 s[24:25], s24, v167
	s_and_b64 s[26:27], s[28:29], s[26:27]
	v_cmp_gt_i32_e64 s[22:23], s22, v167
	s_and_b64 s[24:25], s[26:27], s[24:25]
	s_movk_i32 s18, 0x6b
	v_cmp_gt_i32_e64 s[20:21], s69, v167
	s_and_b64 s[22:23], s[24:25], s[22:23]
	s_movk_i32 s16, 0x6a
	v_cmp_gt_i32_e64 s[18:19], s18, v167
	s_and_b64 s[20:21], s[22:23], s[20:21]
	s_movk_i32 s14, 0x69
	v_cmp_gt_i32_e64 s[16:17], s16, v167
	s_and_b64 s[18:19], s[20:21], s[18:19]
	s_movk_i32 s12, 0x68
	v_cmp_gt_i32_e64 s[14:15], s14, v167
	s_and_b64 s[16:17], s[18:19], s[16:17]
	s_movk_i32 s10, 0x63
	v_cmp_gt_i32_e64 s[12:13], s12, v167
	s_and_b64 s[14:15], s[16:17], s[14:15]
	s_movk_i32 s8, 0x62
	v_cmp_gt_i32_e64 s[10:11], s10, v167
	s_and_b64 s[12:13], s[14:15], s[12:13]
	s_movk_i32 s6, 0x61
	v_cmp_gt_i32_e64 s[8:9], s8, v167
	s_and_b64 s[10:11], s[12:13], s[10:11]
	v_cmp_gt_i32_e64 s[6:7], s6, v167
	s_and_b64 s[8:9], s[10:11], s[8:9]
	s_and_b64 s[6:7], s[8:9], s[6:7]
	s_and_b64 vcc, s[6:7], vcc
	v_cndmask_b32_e64 v78, v78, v160, s[58:59]
	v_cndmask_b32_e64 v77, v77, v160, s[56:57]
	v_cndmask_b32_e64 v76, v76, v160, s[54:55]
	v_cndmask_b32_e64 v75, v75, v160, s[52:53]
	v_cndmask_b32_e64 v74, v74, v160, s[50:51]
	v_cndmask_b32_e64 v73, v73, v160, s[48:49]
	v_cndmask_b32_e64 v72, v72, v160, s[44:45]
	v_cndmask_b32_e64 v71, v71, v160, s[42:43]
	v_cndmask_b32_e64 v70, v70, v160, s[40:41]
	v_cndmask_b32_e64 v69, v69, v160, s[38:39]
	v_cndmask_b32_e64 v68, v68, v160, s[36:37]
	v_cndmask_b32_e64 v67, v67, v160, s[34:35]
	v_cndmask_b32_e64 v95, v95, v160, s[30:31]
	v_cndmask_b32_e64 v94, v94, v160, s[28:29]
	v_cndmask_b32_e64 v93, v93, v160, s[26:27]
	v_cndmask_b32_e64 v92, v92, v160, s[24:25]
	v_cndmask_b32_e64 v91, v91, v160, s[22:23]
	v_cndmask_b32_e64 v90, v90, v160, s[20:21]
	v_cndmask_b32_e64 v89, v89, v160, s[18:19]
	v_cndmask_b32_e64 v88, v88, v160, s[16:17]
	v_cndmask_b32_e64 v87, v87, v160, s[14:15]
	v_cndmask_b32_e64 v86, v86, v160, s[12:13]
	v_cndmask_b32_e64 v85, v85, v160, s[10:11]
	v_cndmask_b32_e64 v84, v84, v160, s[8:9]
	v_cndmask_b32_e64 v83, v83, v160, s[6:7]
	v_cndmask_b32_e32 v82, v82, v160, vcc

.LBB0_243:
	v_cndmask_b32_e64 v120, v117, v116, s[6:7]
	s_waitcnt vmcnt(0)
	v_mul_f32_e32 v116, 0xbe38aa3b, v120
	v_pk_fma_f32 v[80:81], v[80:81], s[84:85], v[116:117] op_sel_hi:[1,0,0]
	v_pk_fma_f32 v[78:79], v[78:79], s[84:85], v[116:117] op_sel_hi:[1,0,0]
	v_pk_fma_f32 v[76:77], v[76:77], s[84:85], v[116:117] op_sel_hi:[1,0,0]
	v_pk_fma_f32 v[74:75], v[74:75], s[84:85], v[116:117] op_sel_hi:[1,0,0]
	v_pk_fma_f32 v[72:73], v[72:73], s[84:85], v[116:117] op_sel_hi:[1,0,0]
	v_pk_fma_f32 v[70:71], v[70:71], s[84:85], v[116:117] op_sel_hi:[1,0,0]
	v_pk_fma_f32 v[68:69], v[68:69], s[84:85], v[116:117] op_sel_hi:[1,0,0]
	v_pk_fma_f32 v[66:67], v[66:67], s[84:85], v[116:117] op_sel_hi:[1,0,0]
	v_pk_fma_f32 v[148:149], v[96:97], s[84:85], v[116:117] op_sel_hi:[1,0,0]
	v_pk_fma_f32 v[150:151], v[94:95], s[84:85], v[116:117] op_sel_hi:[1,0,0]
	v_pk_fma_f32 v[152:153], v[92:93], s[84:85], v[116:117] op_sel_hi:[1,0,0]
	v_pk_fma_f32 v[154:155], v[90:91], s[84:85], v[116:117] op_sel_hi:[1,0,0]
	v_pk_fma_f32 v[180:181], v[88:89], s[84:85], v[116:117] op_sel_hi:[1,0,0]
	v_pk_fma_f32 v[184:185], v[86:87], s[84:85], v[116:117] op_sel_hi:[1,0,0]
	v_pk_fma_f32 v[186:187], v[84:85], s[84:85], v[116:117] op_sel_hi:[1,0,0]
	v_pk_fma_f32 v[116:117], v[82:83], s[84:85], v[116:117] op_sel_hi:[1,0,0]
	v_exp_f32_e32 v196, v66
	v_exp_f32_e32 v197, v67
	v_exp_f32_e32 v198, v68
	v_exp_f32_e32 v199, v69
	v_exp_f32_e32 v200, v70
	v_exp_f32_e32 v201, v71
	v_exp_f32_e32 v202, v72
	v_exp_f32_e32 v203, v73
	v_exp_f32_e32 v204, v74
	v_exp_f32_e32 v205, v75
	v_exp_f32_e32 v206, v76
	v_exp_f32_e32 v207, v77
	v_exp_f32_e32 v208, v78
	v_exp_f32_e32 v209, v79
	v_exp_f32_e32 v210, v80
	v_exp_f32_e32 v211, v81
	s_barrier
	s_add_u32 s6, s90, 0xc0000
	s_addc_u32 s7, s91, 0
	s_mov_b32 m0, s81
	s_nop 0
	global_load_lds_dwordx4 v168, s[6:7] offset:0
	s_add_u32 s6, s92, 0xc0000
	s_addc_u32 s7, s93, 0
	s_cmp_lg_u32 0, -1
	s_cselect_b32 s1, 0, 0
	s_add_i32 s79, s1, s86
	s_add_i32 s78, s79, 0xc000
	s_mov_b32 m0, s78
	s_nop 0
	global_load_lds_dwordx4 v169, s[6:7] offset:0
	s_add_i32 s79, s79, 0xe000
	s_mov_b32 m0, s79
	s_nop 0
	global_load_lds_dwordx4 v170, s[6:7] offset:0
	ds_read_b128 v[66:69], v171
	ds_read_b128 v[70:73], v171 offset:4096
	ds_read_b128 v[122:125], v172
	ds_read_b128 v[126:129], v172 offset:4096
	ds_read_b128 v[130:133], v173
	ds_read_b128 v[134:137], v173 offset:4096
	ds_read_b128 v[140:143], v174
	ds_read_b128 v[144:147], v174 offset:4096
	s_waitcnt lgkmcnt(7)
	v_mfma_f32_32x32x16_bf16 v[82:97], v[66:69], v[110:113], 0
	v_exp_f32_e32 v212, v116
	v_exp_f32_e32 v213, v117
	v_exp_f32_e32 v186, v186
	v_exp_f32_e32 v187, v187
	v_exp_f32_e32 v184, v184
	v_exp_f32_e32 v185, v185
	v_exp_f32_e32 v180, v180
	s_waitcnt lgkmcnt(6)
	v_mfma_f32_32x32x16_bf16 v[66:81], v[70:73], v[110:113], 0
	v_exp_f32_e32 v181, v181
	v_exp_f32_e32 v154, v154
	v_exp_f32_e32 v155, v155
	v_exp_f32_e32 v152, v152
	v_exp_f32_e32 v153, v153
	v_exp_f32_e32 v150, v150
	v_exp_f32_e32 v151, v151
	s_waitcnt lgkmcnt(5)
	v_mfma_f32_32x32x16_bf16 v[82:97], v[122:125], v[106:109], v[82:97]
	v_exp_f32_e32 v148, v148
	v_exp_f32_e32 v149, v149
	v_pk_add_f32 v[116:117], v[206:207], v[152:153]
	v_pk_add_f32 v[122:123], v[198:199], v[186:187]
	v_pk_add_f32 v[214:215], v[196:197], v[212:213]
	v_pk_add_f32 v[124:125], v[210:211], v[148:149]
	v_pk_add_f32 v[216:217], v[208:209], v[150:151]
	s_waitcnt lgkmcnt(4)
	v_mfma_f32_32x32x16_bf16 v[66:81], v[126:129], v[106:109], v[66:81]
	v_pk_add_f32 v[126:127], v[202:203], v[180:181]
	v_pk_add_f32 v[128:129], v[204:205], v[154:155]
	v_pk_add_f32 v[218:219], v[200:201], v[184:185]
	v_pk_add_f32 v[128:129], v[214:215], v[128:129]
	v_pk_add_f32 v[216:217], v[218:219], v[216:217]
	v_pk_add_f32 v[124:125], v[126:127], v[124:125]
	v_pk_add_f32 v[116:117], v[122:123], v[116:117]
	s_waitcnt lgkmcnt(3)
	v_mfma_f32_32x32x16_bf16 v[82:97], v[130:133], v[102:105], v[82:97]
	v_pk_add_f32 v[116:117], v[116:117], v[124:125]
	v_pk_add_f32 v[122:123], v[128:129], v[216:217]
	v_pk_add_f32 v[116:117], v[122:123], v[116:117]
	v_cvt_pk_bf16_f32 v122, v196, v197
	v_cvt_pk_bf16_f32 v123, v198, v199
	v_cvt_pk_bf16_f32 v124, v200, v201
	s_waitcnt lgkmcnt(2)
	v_mfma_f32_32x32x16_bf16 v[66:81], v[134:137], v[102:105], v[66:81]
	v_pk_add_f32 v[116:117], v[116:117], v[116:117] op_sel:[0,1] op_sel_hi:[1,0]
	v_cvt_pk_bf16_f32 v125, v202, v203
	v_cvt_pk_bf16_f32 v126, v204, v205
	v_cvt_pk_bf16_f32 v127, v206, v207
	v_cvt_pk_bf16_f32 v128, v208, v209
	v_cvt_pk_bf16_f32 v129, v210, v211
	s_nop 0
	v_mov_b32_e32 v117, v116
	s_waitcnt lgkmcnt(1)
	v_mfma_f32_32x32x16_bf16 v[82:97], v[140:143], v[98:101], v[82:97]
	v_permlane32_swap_b32_e32 v116, v117
	v_cvt_pk_bf16_f32 v130, v212, v213
	v_cvt_pk_bf16_f32 v131, v186, v187
	v_cvt_pk_bf16_f32 v132, v184, v185
	v_cvt_pk_bf16_f32 v133, v180, v181
	v_cvt_pk_bf16_f32 v134, v154, v155
	s_waitcnt lgkmcnt(0)
	v_mfma_f32_32x32x16_bf16 v[66:81], v[144:147], v[98:101], v[66:81]
	v_cvt_pk_bf16_f32 v135, v152, v153
	v_cvt_pk_bf16_f32 v136, v150, v151
	v_cvt_pk_bf16_f32 v137, v148, v149
	v_permlane32_swap_b32_e32 v122, v124
	v_permlane32_swap_b32_e32 v123, v125
	v_permlane32_swap_b32_e32 v126, v128
	v_permlane32_swap_b32_e32 v127, v129
	v_permlane32_swap_b32_e32 v130, v132
	v_permlane32_swap_b32_e32 v131, v133
	v_permlane32_swap_b32_e32 v134, v136
	v_permlane32_swap_b32_e32 v135, v137
	ds_read_b64_tr_b16 v[140:141], v166 offset:0x4000
	ds_read_b64_tr_b16 v[142:143], v166 offset:0x4800
	ds_read_b64_tr_b16 v[144:145], v166 offset:0x5000
	ds_read_b64_tr_b16 v[146:147], v166 offset:0x5800
	ds_read_b64_tr_b16 v[148:149], v166 offset:0x6000
	ds_read_b64_tr_b16 v[150:151], v166 offset:0x6800
	ds_read_b64_tr_b16 v[152:153], v166 offset:0x7000
	ds_read_b64_tr_b16 v[154:155], v166 offset:0x7800
	ds_read_b64_tr_b16 v[184:185], v166 offset:0x4200
	ds_read_b64_tr_b16 v[186:187], v166 offset:0x4a00
	ds_read_b64_tr_b16 v[196:197], v166 offset:0x5200
	ds_read_b64_tr_b16 v[198:199], v166 offset:0x5a00
	ds_read_b64_tr_b16 v[200:201], v166 offset:0x6200
	ds_read_b64_tr_b16 v[202:203], v166 offset:0x6a00
	ds_read_b64_tr_b16 v[204:205], v166 offset:0x7200
	ds_read_b64_tr_b16 v[206:207], v166 offset:0x7a00
	s_waitcnt lgkmcnt(8)
	s_nop 0
	v_mfma_f32_32x32x16_bf16 v[18:33], v[122:125], v[140:143], v[18:33]
	v_mfma_f32_32x32x16_bf16 v[18:33], v[126:129], v[144:147], v[18:33]
	v_mfma_f32_32x32x16_bf16 v[18:33], v[130:133], v[148:151], v[18:33]
	v_mfma_f32_32x32x16_bf16 v[18:33], v[134:137], v[152:155], v[18:33]
	ds_read_b64_tr_b16 v[140:141], v166 offset:0x4400
	ds_read_b64_tr_b16 v[142:143], v166 offset:0x4c00
	ds_read_b64_tr_b16 v[144:145], v166 offset:0x5400
	ds_read_b64_tr_b16 v[146:147], v166 offset:0x5c00
	ds_read_b64_tr_b16 v[148:149], v166 offset:0x6400
	ds_read_b64_tr_b16 v[150:151], v166 offset:0x6c00
	ds_read_b64_tr_b16 v[152:153], v166 offset:0x7400
	ds_read_b64_tr_b16 v[154:155], v166 offset:0x7c00
	s_waitcnt lgkmcnt(8)
	v_mfma_f32_32x32x16_bf16 v[34:49], v[122:125], v[184:187], v[34:49]
	v_mfma_f32_32x32x16_bf16 v[34:49], v[126:129], v[196:199], v[34:49]
	v_mfma_f32_32x32x16_bf16 v[34:49], v[130:133], v[200:203], v[34:49]
	v_mfma_f32_32x32x16_bf16 v[34:49], v[134:137], v[204:207], v[34:49]
	ds_read_b64_tr_b16 v[184:185], v166 offset:0x4600
	ds_read_b64_tr_b16 v[186:187], v166 offset:0x4e00
	ds_read_b64_tr_b16 v[196:197], v166 offset:0x5600
	ds_read_b64_tr_b16 v[198:199], v166 offset:0x5e00
	ds_read_b64_tr_b16 v[200:201], v166 offset:0x6600
	ds_read_b64_tr_b16 v[202:203], v166 offset:0x6e00
	ds_read_b64_tr_b16 v[204:205], v166 offset:0x7600
	ds_read_b64_tr_b16 v[206:207], v166 offset:0x7e00
	s_waitcnt lgkmcnt(8)
	v_mfma_f32_32x32x16_bf16 v[50:65], v[122:125], v[140:143], v[50:65]
	v_mfma_f32_32x32x16_bf16 v[50:65], v[126:129], v[144:147], v[50:65]
	v_mfma_f32_32x32x16_bf16 v[50:65], v[130:133], v[148:151], v[50:65]
	v_mfma_f32_32x32x16_bf16 v[50:65], v[134:137], v[152:155], v[50:65]
	s_waitcnt lgkmcnt(0)
	v_mfma_f32_32x32x16_bf16 v[2:17], v[122:125], v[184:187], v[2:17]
	s_cmpk_gt_i32 s77, 0xbe
	v_mfma_f32_32x32x16_bf16 v[2:17], v[126:129], v[196:199], v[2:17]
	v_mfma_f32_32x32x16_bf16 v[2:17], v[130:133], v[200:203], v[2:17]
	v_mfma_f32_32x32x16_bf16 v[2:17], v[134:137], v[204:207], v[2:17]
	s_cbranch_scc1 .LBB0_245
	s_movk_i32 s1, 0x80
	v_cmp_gt_i32_e64 s[30:31], s1, v167
	s_movk_i32 s1, 0xa0
	v_cmp_gt_i32_e32 vcc, s1, v167
	s_movk_i32 s1, 0x81
	v_cmp_gt_i32_e64 s[34:35], s1, v167
	s_movk_i32 s1, 0xa1
	v_cmp_gt_i32_e64 s[6:7], s1, v167
	s_movk_i32 s1, 0x82
	v_cmp_gt_i32_e64 s[36:37], s1, v167
	s_movk_i32 s1, 0xa2
	v_cmp_gt_i32_e64 s[8:9], s1, v167
	s_movk_i32 s1, 0x83
	v_cmp_gt_i32_e64 s[38:39], s1, v167
	s_movk_i32 s1, 0xa3
	v_cmp_gt_i32_e64 s[10:11], s1, v167
	s_movk_i32 s1, 0x88
	v_cmp_gt_i32_e64 s[40:41], s1, v167
	s_movk_i32 s1, 0xa8
	v_cmp_gt_i32_e64 s[12:13], s1, v167
	s_movk_i32 s1, 0x89
	v_cmp_gt_i32_e64 s[42:43], s1, v167
	s_movk_i32 s1, 0xa9
	v_cmp_gt_i32_e64 s[14:15], s1, v167
	s_movk_i32 s1, 0x8a
	v_cmp_gt_i32_e64 s[44:45], s1, v167
	s_movk_i32 s1, 0xaa
	v_cmp_gt_i32_e64 s[16:17], s1, v167
	s_movk_i32 s1, 0x8b
	v_cmp_gt_i32_e64 s[48:49], s1, v167
	s_movk_i32 s1, 0xab
	v_cmp_gt_i32_e64 s[18:19], s1, v167
	s_movk_i32 s1, 0x90
	v_cmp_gt_i32_e64 s[50:51], s1, v167
	s_movk_i32 s1, 0xb0
	v_cmp_gt_i32_e64 s[20:21], s1, v167
	s_movk_i32 s1, 0x91
	v_cmp_gt_i32_e64 s[52:53], s1, v167
	s_movk_i32 s1, 0xb1
	v_cmp_gt_i32_e64 s[22:23], s1, v167
	s_movk_i32 s1, 0x92
	v_cmp_gt_i32_e64 s[54:55], s1, v167
	s_movk_i32 s1, 0xb2
	v_cmp_gt_i32_e64 s[24:25], s1, v167
	s_movk_i32 s1, 0x93
	v_cmp_gt_i32_e64 s[56:57], s1, v167
	s_movk_i32 s1, 0xb3
	v_cmp_gt_i32_e64 s[26:27], s1, v167
	s_movk_i32 s1, 0x98
	v_cmp_gt_i32_e64 s[58:59], s1, v167
	s_movk_i32 s1, 0xb8
	v_cmp_gt_i32_e64 s[28:29], s1, v167
	s_movk_i32 s1, 0x9a
	v_cmp_gt_i32_e64 s[60:61], s1, v167
	s_movk_i32 s1, 0x9b
	v_cmp_gt_i32_e64 s[62:63], s1, v167
	s_movk_i32 s1, 0x99
	s_and_b64 s[60:61], s[62:63], s[60:61]
	v_cndmask_b32_e64 v97, v97, v160, s[62:63]
	v_cmp_gt_i32_e64 s[62:63], s1, v167
	v_cndmask_b32_e64 v96, v96, v160, s[60:61]
	s_and_b64 s[60:61], s[60:61], s[62:63]
	s_and_b64 s[58:59], s[60:61], s[58:59]
	s_and_b64 s[56:57], s[58:59], s[56:57]
	s_and_b64 s[54:55], s[56:57], s[54:55]
	s_and_b64 s[52:53], s[54:55], s[52:53]
	s_and_b64 s[50:51], s[52:53], s[50:51]
	s_and_b64 s[48:49], s[50:51], s[48:49]
	s_and_b64 s[44:45], s[48:49], s[44:45]
	s_and_b64 s[42:43], s[44:45], s[42:43]
	s_and_b64 s[40:41], s[42:43], s[40:41]
	s_and_b64 s[38:39], s[40:41], s[38:39]
	s_movk_i32 s1, 0xb9
	s_and_b64 s[36:37], s[38:39], s[36:37]
	v_cmp_gt_i32_e64 s[62:63], s1, v167
	s_movk_i32 s1, 0xba
	s_and_b64 s[34:35], s[36:37], s[34:35]
	v_cndmask_b32_e64 v95, v95, v160, s[60:61]
	v_cmp_gt_i32_e64 s[60:61], s1, v167
	s_and_b64 s[30:31], s[34:35], s[30:31]
	s_movk_i32 s1, 0xbb
	v_cndmask_b32_e64 v82, v82, v160, s[30:31]
	v_cmp_gt_i32_e64 s[30:31], s1, v167
	v_cndmask_b32_e64 v94, v94, v160, s[58:59]
	v_cndmask_b32_e64 v93, v93, v160, s[56:57]
	v_cndmask_b32_e64 v81, v81, v160, s[30:31]
	s_and_b64 s[30:31], s[30:31], s[60:61]
	v_cndmask_b32_e64 v80, v80, v160, s[30:31]
	s_and_b64 s[30:31], s[30:31], s[62:63]
	s_and_b64 s[28:29], s[30:31], s[28:29]
	s_and_b64 s[26:27], s[28:29], s[26:27]
	s_and_b64 s[24:25], s[26:27], s[24:25]
	s_and_b64 s[22:23], s[24:25], s[22:23]
	s_and_b64 s[20:21], s[22:23], s[20:21]
	s_and_b64 s[18:19], s[20:21], s[18:19]
	s_and_b64 s[16:17], s[18:19], s[16:17]
	s_and_b64 s[14:15], s[16:17], s[14:15]
	s_and_b64 s[12:13], s[14:15], s[12:13]
	s_and_b64 s[10:11], s[12:13], s[10:11]
	s_and_b64 s[8:9], s[10:11], s[8:9]
	s_and_b64 s[6:7], s[8:9], s[6:7]
	s_and_b64 vcc, s[6:7], vcc
	v_cndmask_b32_e64 v92, v92, v160, s[54:55]
	v_cndmask_b32_e64 v91, v91, v160, s[52:53]
	v_cndmask_b32_e64 v90, v90, v160, s[50:51]
	v_cndmask_b32_e64 v89, v89, v160, s[48:49]
	v_cndmask_b32_e64 v88, v88, v160, s[44:45]
	v_cndmask_b32_e64 v87, v87, v160, s[42:43]
	v_cndmask_b32_e64 v86, v86, v160, s[40:41]
	v_cndmask_b32_e64 v85, v85, v160, s[38:39]
	v_cndmask_b32_e64 v84, v84, v160, s[36:37]
	v_cndmask_b32_e64 v83, v83, v160, s[34:35]
	v_cndmask_b32_e64 v79, v79, v160, s[30:31]
	v_cndmask_b32_e64 v78, v78, v160, s[28:29]
	v_cndmask_b32_e64 v77, v77, v160, s[26:27]
	v_cndmask_b32_e64 v76, v76, v160, s[24:25]
	v_cndmask_b32_e64 v75, v75, v160, s[22:23]
	v_cndmask_b32_e64 v74, v74, v160, s[20:21]
	v_cndmask_b32_e64 v73, v73, v160, s[18:19]
	v_cndmask_b32_e64 v72, v72, v160, s[16:17]
	v_cndmask_b32_e64 v71, v71, v160, s[14:15]
	v_cndmask_b32_e64 v70, v70, v160, s[12:13]
	v_cndmask_b32_e64 v69, v69, v160, s[10:11]
	v_cndmask_b32_e64 v68, v68, v160, s[8:9]
	v_cndmask_b32_e64 v67, v67, v160, s[6:7]
	v_cndmask_b32_e32 v66, v66, v160, vcc

.LBB0_251:
	.p2align 3
	s_nop 0
	s_add_u32 s72, s90, s70
	s_addc_u32 s73, s91, s71
	s_add_u32 s6, s72, 0x100000
	s_addc_u32 s7, s73, 0
	s_add_u32 s88, s92, s70
	s_addc_u32 s89, s93, s71
	s_mov_b32 m0, s85
	s_nop 0
	global_load_lds_dwordx4 v168, s[6:7] offset:0
	s_add_u32 s6, s88, 0x100000
	s_addc_u32 s7, s89, 0
	s_mov_b32 m0, s86
	s_nop 0
	global_load_lds_dwordx4 v169, s[6:7] offset:0
	s_nop 0
	s_mov_b32 m0, s87
	s_nop 0
	global_load_lds_dwordx4 v170, s[6:7] offset:0
	ds_read_b128 v[66:69], v175
	ds_read_b128 v[82:85], v175 offset:4096
	ds_read_b128 v[114:117], v176
	ds_read_b128 v[184:187], v176 offset:4096
	ds_read_b128 v[196:199], v177
	ds_read_b128 v[200:203], v177 offset:4096
	ds_read_b128 v[204:207], v178
	ds_read_b128 v[208:211], v178 offset:4096
	s_waitcnt lgkmcnt(7)
	v_mfma_f32_32x32x16_bf16 v[66:81], v[66:69], v[110:113], 0
	v_exp_f32_e32 v120, v154
	v_exp_f32_e32 v121, v155
	v_exp_f32_e32 v152, v152
	v_exp_f32_e32 v153, v153
	v_exp_f32_e32 v150, v150
	v_exp_f32_e32 v151, v151
	v_exp_f32_e32 v148, v148
	s_waitcnt lgkmcnt(6)
	v_mfma_f32_32x32x16_bf16 v[82:97], v[82:85], v[110:113], 0
	v_exp_f32_e32 v149, v149
	v_exp_f32_e32 v146, v146
	v_exp_f32_e32 v147, v147
	v_exp_f32_e32 v144, v144
	v_exp_f32_e32 v145, v145
	v_exp_f32_e32 v154, v140
	v_exp_f32_e32 v155, v141
	s_waitcnt lgkmcnt(5)
	v_mfma_f32_32x32x16_bf16 v[66:81], v[114:117], v[106:109], v[66:81]
	v_exp_f32_e32 v116, v142
	v_exp_f32_e32 v117, v143
	v_pk_add_f32 v[114:115], v[126:127], v[144:145]
	v_pk_add_f32 v[140:141], v[134:135], v[152:153]
	v_pk_add_f32 v[142:143], v[122:123], v[154:155]
	v_pk_add_f32 v[212:213], v[136:137], v[120:121]
	v_pk_add_f32 v[214:215], v[124:125], v[116:117]
	s_waitcnt lgkmcnt(4)
	v_mfma_f32_32x32x16_bf16 v[82:97], v[184:187], v[106:109], v[82:97]
	v_pk_add_f32 v[184:185], v[130:131], v[148:149]
	v_pk_add_f32 v[186:187], v[128:129], v[146:147]
	v_pk_add_f32 v[216:217], v[132:133], v[150:151]
	v_pk_add_f32 v[186:187], v[212:213], v[186:187]
	v_pk_add_f32 v[214:215], v[216:217], v[214:215]
	v_pk_add_f32 v[142:143], v[184:185], v[142:143]
	v_pk_add_f32 v[114:115], v[140:141], v[114:115]
	s_waitcnt lgkmcnt(3)
	v_mfma_f32_32x32x16_bf16 v[66:81], v[196:199], v[102:105], v[66:81]
	v_pk_add_f32 v[114:115], v[114:115], v[142:143]
	v_pk_add_f32 v[140:141], v[186:187], v[214:215]
	v_pk_add_f32 v[114:115], v[140:141], v[114:115]
	v_cvt_pk_bf16_f32 v140, v136, v137
	v_cvt_pk_bf16_f32 v141, v134, v135
	v_cvt_pk_bf16_f32 v142, v132, v133
	s_waitcnt lgkmcnt(2)
	v_mfma_f32_32x32x16_bf16 v[82:97], v[200:203], v[102:105], v[82:97]
	v_pk_add_f32 v[114:115], v[114:115], v[114:115] op_sel:[0,1] op_sel_hi:[1,0]
	v_cvt_pk_bf16_f32 v143, v130, v131
	v_cvt_pk_bf16_f32 v128, v128, v129
	v_cvt_pk_bf16_f32 v129, v126, v127
	v_cvt_pk_bf16_f32 v130, v124, v125
	v_cvt_pk_bf16_f32 v131, v122, v123
	s_nop 0
	v_mov_b32_e32 v115, v114
	s_waitcnt lgkmcnt(1)
	v_mfma_f32_32x32x16_bf16 v[66:81], v[204:207], v[98:101], v[66:81]
	v_permlane32_swap_b32_e32 v114, v115
	v_cvt_pk_bf16_f32 v120, v120, v121
	v_cvt_pk_bf16_f32 v121, v152, v153
	v_cvt_pk_bf16_f32 v122, v150, v151
	v_cvt_pk_bf16_f32 v123, v148, v149
	v_cvt_pk_bf16_f32 v124, v146, v147
	s_waitcnt lgkmcnt(0)
	v_mfma_f32_32x32x16_bf16 v[82:97], v[208:211], v[98:101], v[82:97]
	v_cvt_pk_bf16_f32 v125, v144, v145
	v_cvt_pk_bf16_f32 v126, v116, v117
	v_cvt_pk_bf16_f32 v127, v154, v155
	v_permlane32_swap_b32_e32 v140, v142
	v_permlane32_swap_b32_e32 v141, v143
	v_permlane32_swap_b32_e32 v128, v130
	v_permlane32_swap_b32_e32 v129, v131
	v_permlane32_swap_b32_e32 v120, v122
	v_permlane32_swap_b32_e32 v121, v123
	v_permlane32_swap_b32_e32 v124, v126
	v_permlane32_swap_b32_e32 v125, v127
	ds_read_b64_tr_b16 v[132:133], v166 offset:0x8000
	ds_read_b64_tr_b16 v[134:135], v166 offset:0x8800
	ds_read_b64_tr_b16 v[144:145], v166 offset:0x9000
	ds_read_b64_tr_b16 v[146:147], v166 offset:0x9800
	ds_read_b64_tr_b16 v[148:149], v166 offset:0xa000
	ds_read_b64_tr_b16 v[150:151], v166 offset:0xa800
	ds_read_b64_tr_b16 v[152:153], v166 offset:0xb000
	ds_read_b64_tr_b16 v[154:155], v166 offset:0xb800
	ds_read_b64_tr_b16 v[184:185], v166 offset:0x8200
	ds_read_b64_tr_b16 v[186:187], v166 offset:0x8a00
	ds_read_b64_tr_b16 v[196:197], v166 offset:0x9200
	ds_read_b64_tr_b16 v[198:199], v166 offset:0x9a00
	ds_read_b64_tr_b16 v[200:201], v166 offset:0xa200
	ds_read_b64_tr_b16 v[202:203], v166 offset:0xaa00
	ds_read_b64_tr_b16 v[204:205], v166 offset:0xb200
	ds_read_b64_tr_b16 v[206:207], v166 offset:0xba00
	s_waitcnt lgkmcnt(8)
	s_nop 0
	v_mfma_f32_32x32x16_bf16 v[18:33], v[140:143], v[132:135], v[18:33]
	v_mfma_f32_32x32x16_bf16 v[18:33], v[128:131], v[144:147], v[18:33]
	v_mfma_f32_32x32x16_bf16 v[18:33], v[120:123], v[148:151], v[18:33]
	v_mfma_f32_32x32x16_bf16 v[18:33], v[124:127], v[152:155], v[18:33]
	ds_read_b64_tr_b16 v[132:133], v166 offset:0x8400
	ds_read_b64_tr_b16 v[134:135], v166 offset:0x8c00
	ds_read_b64_tr_b16 v[144:145], v166 offset:0x9400
	ds_read_b64_tr_b16 v[146:147], v166 offset:0x9c00
	ds_read_b64_tr_b16 v[148:149], v166 offset:0xa400
	ds_read_b64_tr_b16 v[150:151], v166 offset:0xac00
	ds_read_b64_tr_b16 v[152:153], v166 offset:0xb400
	ds_read_b64_tr_b16 v[154:155], v166 offset:0xbc00
	s_waitcnt lgkmcnt(8)
	v_mfma_f32_32x32x16_bf16 v[34:49], v[140:143], v[184:187], v[34:49]
	v_mfma_f32_32x32x16_bf16 v[34:49], v[128:131], v[196:199], v[34:49]
	v_mfma_f32_32x32x16_bf16 v[34:49], v[120:123], v[200:203], v[34:49]
	v_mfma_f32_32x32x16_bf16 v[34:49], v[124:127], v[204:207], v[34:49]
	ds_read_b64_tr_b16 v[184:185], v166 offset:0x8600
	ds_read_b64_tr_b16 v[186:187], v166 offset:0x8e00
	ds_read_b64_tr_b16 v[196:197], v166 offset:0x9600
	ds_read_b64_tr_b16 v[198:199], v166 offset:0x9e00
	ds_read_b64_tr_b16 v[200:201], v166 offset:0xa600
	ds_read_b64_tr_b16 v[202:203], v166 offset:0xae00
	ds_read_b64_tr_b16 v[204:205], v166 offset:0xb600
	ds_read_b64_tr_b16 v[206:207], v166 offset:0xbe00
	s_waitcnt lgkmcnt(8)
	v_mfma_f32_32x32x16_bf16 v[50:65], v[140:143], v[132:135], v[50:65]
	v_mfma_f32_32x32x16_bf16 v[50:65], v[128:131], v[144:147], v[50:65]
	v_mfma_f32_32x32x16_bf16 v[50:65], v[120:123], v[148:151], v[50:65]
	v_mfma_f32_32x32x16_bf16 v[50:65], v[124:127], v[152:155], v[50:65]
	s_waitcnt lgkmcnt(0)
	v_mfma_f32_32x32x16_bf16 v[2:17], v[140:143], v[184:187], v[2:17]
	s_add_i32 s6, s95, 0xffffff40
	s_cmp_le_i32 s6, s77
	v_mfma_f32_32x32x16_bf16 v[2:17], v[128:131], v[196:199], v[2:17]
	v_mfma_f32_32x32x16_bf16 v[2:17], v[120:123], v[200:203], v[2:17]
	v_mfma_f32_32x32x16_bf16 v[2:17], v[124:127], v[204:207], v[2:17]
	s_cbranch_scc1 .LBB0_253
	v_cmp_gt_i32_e64 s[66:67], 26, v183
	v_cmp_gt_i32_e64 s[68:69], 27, v183
	v_cmp_gt_i32_e64 s[64:65], 25, v183
	s_and_b64 s[66:67], s[68:69], s[66:67]
	v_cmp_gt_i32_e64 s[62:63], 24, v183
	s_and_b64 s[64:65], s[66:67], s[64:65]
	v_cmp_gt_i32_e64 s[60:61], 19, v183
	s_and_b64 s[62:63], s[64:65], s[62:63]
	v_cmp_gt_i32_e64 s[58:59], 18, v183
	s_and_b64 s[60:61], s[62:63], s[60:61]
	v_cmp_gt_i32_e64 s[56:57], 17, v183
	s_and_b64 s[58:59], s[60:61], s[58:59]
	v_cmp_gt_i32_e64 s[54:55], 16, v183
	s_and_b64 s[56:57], s[58:59], s[56:57]
	v_cmp_gt_i32_e64 s[52:53], 11, v183
	s_and_b64 s[54:55], s[56:57], s[54:55]
	v_cmp_gt_i32_e64 s[50:51], 10, v183
	s_and_b64 s[52:53], s[54:55], s[52:53]
	v_cmp_gt_i32_e64 s[48:49], 9, v183
	s_and_b64 s[50:51], s[52:53], s[50:51]
	v_cmp_gt_i32_e64 s[44:45], 8, v183
	s_and_b64 s[48:49], s[50:51], s[48:49]
	v_cmp_gt_i32_e64 s[42:43], 3, v183
	s_and_b64 s[44:45], s[48:49], s[44:45]
	v_cmp_gt_i32_e64 s[40:41], 2, v183
	s_and_b64 s[42:43], s[44:45], s[42:43]
	v_cmp_gt_i32_e64 s[38:39], 1, v183
	s_and_b64 s[40:41], s[42:43], s[40:41]
	v_cmp_gt_i32_e64 s[36:37], 0, v183
	s_and_b64 s[38:39], s[40:41], s[38:39]
	s_and_b64 s[36:37], s[38:39], s[36:37]
	v_cmp_gt_i32_e64 s[34:35], 58, v183
	v_cndmask_b32_e64 v66, v66, v160, s[36:37]
	v_cmp_gt_i32_e64 s[36:37], 59, v183
	v_cmp_gt_i32_e64 s[30:31], 57, v183
	s_and_b64 s[34:35], s[36:37], s[34:35]
	v_cmp_gt_i32_e64 s[28:29], 56, v183
	s_and_b64 s[30:31], s[34:35], s[30:31]
	v_cmp_gt_i32_e64 s[26:27], 51, v183
	s_and_b64 s[28:29], s[30:31], s[28:29]
	v_cmp_gt_i32_e64 s[24:25], 50, v183
	s_and_b64 s[26:27], s[28:29], s[26:27]
	v_cmp_gt_i32_e64 s[22:23], 49, v183
	s_and_b64 s[24:25], s[26:27], s[24:25]
	v_cmp_gt_i32_e64 s[20:21], 48, v183
	s_and_b64 s[22:23], s[24:25], s[22:23]
	v_cmp_gt_i32_e64 s[18:19], 43, v183
	s_and_b64 s[20:21], s[22:23], s[20:21]
	v_cmp_gt_i32_e64 s[16:17], 42, v183
	s_and_b64 s[18:19], s[20:21], s[18:19]
	v_cmp_gt_i32_e64 s[14:15], 41, v183
	s_and_b64 s[16:17], s[18:19], s[16:17]
	v_cmp_gt_i32_e64 s[12:13], 40, v183
	s_and_b64 s[14:15], s[16:17], s[14:15]
	v_cmp_gt_i32_e64 s[10:11], 35, v183
	s_and_b64 s[12:13], s[14:15], s[12:13]
	v_cmp_gt_i32_e64 s[8:9], 34, v183
	s_and_b64 s[10:11], s[12:13], s[10:11]
	v_cmp_gt_i32_e64 s[6:7], 33, v183
	s_and_b64 s[8:9], s[10:11], s[8:9]
	v_cmp_gt_i32_e32 vcc, 32, v183
	s_and_b64 s[6:7], s[8:9], s[6:7]
	s_and_b64 vcc, s[6:7], vcc
	v_cndmask_b32_e64 v81, v81, v160, s[68:69]
	v_cndmask_b32_e64 v80, v80, v160, s[66:67]
	v_cndmask_b32_e64 v79, v79, v160, s[64:65]
	v_cndmask_b32_e64 v78, v78, v160, s[62:63]
	v_cndmask_b32_e64 v77, v77, v160, s[60:61]
	v_cndmask_b32_e64 v76, v76, v160, s[58:59]
	v_cndmask_b32_e64 v75, v75, v160, s[56:57]
	v_cndmask_b32_e64 v74, v74, v160, s[54:55]
	v_cndmask_b32_e64 v73, v73, v160, s[52:53]
	v_cndmask_b32_e64 v72, v72, v160, s[50:51]
	v_cndmask_b32_e64 v71, v71, v160, s[48:49]
	v_cndmask_b32_e64 v70, v70, v160, s[44:45]
	v_cndmask_b32_e64 v69, v69, v160, s[42:43]
	v_cndmask_b32_e64 v68, v68, v160, s[40:41]
	v_cndmask_b32_e64 v67, v67, v160, s[38:39]
	v_cndmask_b32_e64 v97, v97, v160, s[36:37]
	v_cndmask_b32_e64 v96, v96, v160, s[34:35]
	v_cndmask_b32_e64 v95, v95, v160, s[30:31]
	v_cndmask_b32_e64 v94, v94, v160, s[28:29]
	v_cndmask_b32_e64 v93, v93, v160, s[26:27]
	v_cndmask_b32_e64 v92, v92, v160, s[24:25]
	v_cndmask_b32_e64 v91, v91, v160, s[22:23]
	v_cndmask_b32_e64 v90, v90, v160, s[20:21]
	v_cndmask_b32_e64 v89, v89, v160, s[18:19]
	v_cndmask_b32_e64 v88, v88, v160, s[16:17]
	v_cndmask_b32_e64 v87, v87, v160, s[14:15]
	v_cndmask_b32_e64 v86, v86, v160, s[12:13]
	v_cndmask_b32_e64 v85, v85, v160, s[10:11]
	v_cndmask_b32_e64 v84, v84, v160, s[8:9]
	v_cndmask_b32_e64 v83, v83, v160, s[6:7]
	v_cndmask_b32_e32 v82, v82, v160, vcc

.LBB0_257:
	v_cndmask_b32_e64 v120, v116, v139, s[6:7]
	s_waitcnt vmcnt(0)
	v_mul_f32_e32 v116, 0xbe38aa3b, v120
	v_pk_fma_f32 v[80:81], v[80:81], s[84:85], v[116:117] op_sel_hi:[1,0,0]
	v_pk_fma_f32 v[78:79], v[78:79], s[84:85], v[116:117] op_sel_hi:[1,0,0]
	v_pk_fma_f32 v[76:77], v[76:77], s[84:85], v[116:117] op_sel_hi:[1,0,0]
	v_pk_fma_f32 v[74:75], v[74:75], s[84:85], v[116:117] op_sel_hi:[1,0,0]
	v_pk_fma_f32 v[72:73], v[72:73], s[84:85], v[116:117] op_sel_hi:[1,0,0]
	v_pk_fma_f32 v[70:71], v[70:71], s[84:85], v[116:117] op_sel_hi:[1,0,0]
	v_pk_fma_f32 v[68:69], v[68:69], s[84:85], v[116:117] op_sel_hi:[1,0,0]
	v_pk_fma_f32 v[66:67], v[66:67], s[84:85], v[116:117] op_sel_hi:[1,0,0]
	v_pk_fma_f32 v[154:155], v[88:89], s[84:85], v[116:117] op_sel_hi:[1,0,0]
	v_pk_fma_f32 v[186:187], v[86:87], s[84:85], v[116:117] op_sel_hi:[1,0,0]
	v_pk_fma_f32 v[86:87], v[84:85], s[84:85], v[116:117] op_sel_hi:[1,0,0]
	v_pk_fma_f32 v[88:89], v[82:83], s[84:85], v[116:117] op_sel_hi:[1,0,0]
	v_pk_fma_f32 v[146:147], v[96:97], s[84:85], v[116:117] op_sel_hi:[1,0,0]
	v_pk_fma_f32 v[148:149], v[94:95], s[84:85], v[116:117] op_sel_hi:[1,0,0]
	v_pk_fma_f32 v[150:151], v[92:93], s[84:85], v[116:117] op_sel_hi:[1,0,0]
	v_pk_fma_f32 v[152:153], v[90:91], s[84:85], v[116:117] op_sel_hi:[1,0,0]
	v_exp_f32_e32 v196, v66
	v_exp_f32_e32 v197, v67
	v_exp_f32_e32 v198, v68
	v_exp_f32_e32 v199, v69
	v_exp_f32_e32 v200, v70
	v_exp_f32_e32 v201, v71
	v_exp_f32_e32 v202, v72
	v_exp_f32_e32 v203, v73
	v_exp_f32_e32 v204, v74
	v_exp_f32_e32 v205, v75
	v_exp_f32_e32 v206, v76
	v_exp_f32_e32 v207, v77
	v_exp_f32_e32 v208, v78
	v_exp_f32_e32 v209, v79
	v_exp_f32_e32 v210, v80
	v_exp_f32_e32 v211, v81
	s_barrier
	s_add_u32 s6, s72, 0x140000
	s_addc_u32 s7, s73, 0
	s_mov_b32 m0, s81
	s_nop 0
	global_load_lds_dwordx4 v168, s[6:7] offset:0
	s_add_u32 s6, s88, 0x140000
	s_addc_u32 s7, s89, 0
	s_mov_b32 m0, s74
	s_nop 0
	global_load_lds_dwordx4 v169, s[6:7] offset:0
	s_nop 0
	s_mov_b32 m0, s0
	s_nop 0
	global_load_lds_dwordx4 v170, s[6:7] offset:0
	ds_read_b128 v[66:69], v171
	ds_read_b128 v[82:85], v171 offset:4096
	ds_read_b128 v[122:125], v172
	ds_read_b128 v[126:129], v172 offset:4096
	v_exp_f32_e32 v212, v88
	s_waitcnt lgkmcnt(3)
	v_mfma_f32_32x32x16_bf16 v[66:81], v[66:69], v[110:113], 0
	v_exp_f32_e32 v213, v89
	v_exp_f32_e32 v214, v86
	v_exp_f32_e32 v215, v87
	ds_read_b128 v[130:133], v173
	ds_read_b128 v[134:137], v173 offset:4096
	ds_read_b128 v[138:141], v174
	ds_read_b128 v[142:145], v174 offset:4096
	v_exp_f32_e32 v186, v186
	v_exp_f32_e32 v187, v187
	v_exp_f32_e32 v154, v154
	s_waitcnt lgkmcnt(6)
	v_mfma_f32_32x32x16_bf16 v[82:97], v[82:85], v[110:113], 0
	v_exp_f32_e32 v155, v155
	v_exp_f32_e32 v152, v152
	v_exp_f32_e32 v153, v153
	v_exp_f32_e32 v150, v150
	v_exp_f32_e32 v151, v151
	v_exp_f32_e32 v148, v148
	v_exp_f32_e32 v149, v149
	s_waitcnt lgkmcnt(5)
	v_mfma_f32_32x32x16_bf16 v[66:81], v[122:125], v[106:109], v[66:81]
	v_exp_f32_e32 v146, v146
	v_exp_f32_e32 v147, v147
	v_pk_add_f32 v[116:117], v[206:207], v[150:151]
	v_pk_add_f32 v[122:123], v[198:199], v[214:215]
	v_pk_add_f32 v[216:217], v[196:197], v[212:213]
	v_pk_add_f32 v[124:125], v[210:211], v[146:147]
	v_pk_add_f32 v[218:219], v[208:209], v[148:149]
	s_waitcnt lgkmcnt(4)
	v_mfma_f32_32x32x16_bf16 v[82:97], v[126:129], v[106:109], v[82:97]
	v_pk_add_f32 v[126:127], v[202:203], v[154:155]
	v_pk_add_f32 v[128:129], v[204:205], v[152:153]
	v_pk_add_f32 v[220:221], v[200:201], v[186:187]
	v_pk_add_f32 v[128:129], v[216:217], v[128:129]
	v_pk_add_f32 v[218:219], v[220:221], v[218:219]
	v_pk_add_f32 v[124:125], v[126:127], v[124:125]
	v_pk_add_f32 v[116:117], v[122:123], v[116:117]
	s_waitcnt lgkmcnt(3)
	v_mfma_f32_32x32x16_bf16 v[66:81], v[130:133], v[102:105], v[66:81]
	v_pk_add_f32 v[116:117], v[116:117], v[124:125]
	v_pk_add_f32 v[122:123], v[128:129], v[218:219]
	v_pk_add_f32 v[116:117], v[122:123], v[116:117]
	v_cvt_pk_bf16_f32 v122, v196, v197
	v_cvt_pk_bf16_f32 v123, v198, v199
	v_cvt_pk_bf16_f32 v124, v200, v201
	s_waitcnt lgkmcnt(2)
	v_mfma_f32_32x32x16_bf16 v[82:97], v[134:137], v[102:105], v[82:97]
	v_pk_add_f32 v[116:117], v[116:117], v[116:117] op_sel:[0,1] op_sel_hi:[1,0]
	v_cvt_pk_bf16_f32 v125, v202, v203
	v_cvt_pk_bf16_f32 v126, v204, v205
	v_cvt_pk_bf16_f32 v127, v206, v207
	v_cvt_pk_bf16_f32 v128, v208, v209
	v_cvt_pk_bf16_f32 v129, v210, v211
	s_nop 0
	v_mov_b32_e32 v117, v116
	s_waitcnt lgkmcnt(1)
	v_mfma_f32_32x32x16_bf16 v[66:81], v[138:141], v[98:101], v[66:81]
	v_permlane32_swap_b32_e32 v116, v117
	v_cvt_pk_bf16_f32 v130, v212, v213
	v_cvt_pk_bf16_f32 v131, v214, v215
	v_cvt_pk_bf16_f32 v132, v186, v187
	v_cvt_pk_bf16_f32 v133, v154, v155
	v_cvt_pk_bf16_f32 v134, v152, v153
	s_waitcnt lgkmcnt(0)
	v_mfma_f32_32x32x16_bf16 v[82:97], v[142:145], v[98:101], v[82:97]
	v_cvt_pk_bf16_f32 v135, v150, v151
	v_cvt_pk_bf16_f32 v136, v148, v149
	v_cvt_pk_bf16_f32 v137, v146, v147
	v_permlane32_swap_b32_e32 v122, v124
	v_permlane32_swap_b32_e32 v123, v125
	v_permlane32_swap_b32_e32 v126, v128
	v_permlane32_swap_b32_e32 v127, v129
	v_permlane32_swap_b32_e32 v130, v132
	v_permlane32_swap_b32_e32 v131, v133
	v_permlane32_swap_b32_e32 v134, v136
	v_permlane32_swap_b32_e32 v135, v137
	ds_read_b64_tr_b16 v[138:139], v166 offset:0xc000
	ds_read_b64_tr_b16 v[140:141], v166 offset:0xc800
	ds_read_b64_tr_b16 v[142:143], v166 offset:0xd000
	ds_read_b64_tr_b16 v[144:145], v166 offset:0xd800
	ds_read_b64_tr_b16 v[146:147], v166 offset:0xe000
	ds_read_b64_tr_b16 v[148:149], v166 offset:0xe800
	ds_read_b64_tr_b16 v[150:151], v166 offset:0xf000
	ds_read_b64_tr_b16 v[152:153], v166 offset:0xf800
	ds_read_b64_tr_b16 v[196:197], v166 offset:0xc200
	ds_read_b64_tr_b16 v[198:199], v166 offset:0xca00
	ds_read_b64_tr_b16 v[200:201], v166 offset:0xd200
	ds_read_b64_tr_b16 v[202:203], v166 offset:0xda00
	ds_read_b64_tr_b16 v[204:205], v166 offset:0xe200
	ds_read_b64_tr_b16 v[206:207], v166 offset:0xea00
	ds_read_b64_tr_b16 v[208:209], v166 offset:0xf200
	ds_read_b64_tr_b16 v[210:211], v166 offset:0xfa00
	s_waitcnt lgkmcnt(8)
	s_nop 0
	v_mfma_f32_32x32x16_bf16 v[18:33], v[122:125], v[138:141], v[18:33]
	v_mfma_f32_32x32x16_bf16 v[18:33], v[126:129], v[142:145], v[18:33]
	v_mfma_f32_32x32x16_bf16 v[18:33], v[130:133], v[146:149], v[18:33]
	v_mfma_f32_32x32x16_bf16 v[18:33], v[134:137], v[150:153], v[18:33]
	ds_read_b64_tr_b16 v[138:139], v166 offset:0xc400
	ds_read_b64_tr_b16 v[140:141], v166 offset:0xcc00
	ds_read_b64_tr_b16 v[142:143], v166 offset:0xd400
	ds_read_b64_tr_b16 v[144:145], v166 offset:0xdc00
	ds_read_b64_tr_b16 v[146:147], v166 offset:0xe400
	ds_read_b64_tr_b16 v[148:149], v166 offset:0xec00
	ds_read_b64_tr_b16 v[150:151], v166 offset:0xf400
	ds_read_b64_tr_b16 v[152:153], v166 offset:0xfc00
	s_waitcnt lgkmcnt(8)
	v_mfma_f32_32x32x16_bf16 v[34:49], v[122:125], v[196:199], v[34:49]
	v_mfma_f32_32x32x16_bf16 v[34:49], v[126:129], v[200:203], v[34:49]
	v_mfma_f32_32x32x16_bf16 v[34:49], v[130:133], v[204:207], v[34:49]
	v_mfma_f32_32x32x16_bf16 v[34:49], v[134:137], v[208:211], v[34:49]
	ds_read_b64_tr_b16 v[196:197], v166 offset:0xc600
	ds_read_b64_tr_b16 v[198:199], v166 offset:0xce00
	ds_read_b64_tr_b16 v[200:201], v166 offset:0xd600
	ds_read_b64_tr_b16 v[202:203], v166 offset:0xde00
	ds_read_b64_tr_b16 v[204:205], v166 offset:0xe600
	ds_read_b64_tr_b16 v[206:207], v166 offset:0xee00
	ds_read_b64_tr_b16 v[208:209], v166 offset:0xf600
	ds_read_b64_tr_b16 v[210:211], v166 offset:0xfe00
	s_waitcnt lgkmcnt(8)
	v_mfma_f32_32x32x16_bf16 v[50:65], v[122:125], v[138:141], v[50:65]
	v_mfma_f32_32x32x16_bf16 v[50:65], v[126:129], v[142:145], v[50:65]
	v_mfma_f32_32x32x16_bf16 v[50:65], v[130:133], v[146:149], v[50:65]
	v_mfma_f32_32x32x16_bf16 v[50:65], v[134:137], v[150:153], v[50:65]
	s_waitcnt lgkmcnt(0)
	v_mfma_f32_32x32x16_bf16 v[2:17], v[122:125], v[196:199], v[2:17]
	s_add_i32 s6, s95, 0xffffff80
	s_cmp_le_i32 s6, s77
	v_mfma_f32_32x32x16_bf16 v[2:17], v[126:129], v[200:203], v[2:17]
	v_mfma_f32_32x32x16_bf16 v[2:17], v[130:133], v[204:207], v[2:17]
	v_mfma_f32_32x32x16_bf16 v[2:17], v[134:137], v[208:211], v[2:17]
	s_cbranch_scc1 .LBB0_259
	v_subrev_u32_e32 v121, 64, v183
	v_cmp_gt_i32_e64 s[66:67], 26, v121
	v_cmp_gt_i32_e64 s[68:69], 27, v121
	v_cmp_gt_i32_e64 s[64:65], 25, v121
	s_and_b64 s[66:67], s[68:69], s[66:67]
	v_cmp_gt_i32_e64 s[62:63], 24, v121
	s_and_b64 s[64:65], s[66:67], s[64:65]
	v_cmp_gt_i32_e64 s[60:61], 19, v121
	s_and_b64 s[62:63], s[64:65], s[62:63]
	v_cmp_gt_i32_e64 s[58:59], 18, v121
	s_and_b64 s[60:61], s[62:63], s[60:61]
	v_cmp_gt_i32_e64 s[56:57], 17, v121
	s_and_b64 s[58:59], s[60:61], s[58:59]
	v_cmp_gt_i32_e64 s[54:55], 16, v121
	s_and_b64 s[56:57], s[58:59], s[56:57]
	v_cmp_gt_i32_e64 s[52:53], 11, v121
	s_and_b64 s[54:55], s[56:57], s[54:55]
	v_cmp_gt_i32_e64 s[50:51], 10, v121
	s_and_b64 s[52:53], s[54:55], s[52:53]
	v_cmp_gt_i32_e64 s[48:49], 9, v121
	s_and_b64 s[50:51], s[52:53], s[50:51]
	v_cmp_gt_i32_e64 s[44:45], 8, v121
	s_and_b64 s[48:49], s[50:51], s[48:49]
	v_cmp_gt_i32_e64 s[42:43], 3, v121
	s_and_b64 s[44:45], s[48:49], s[44:45]
	v_cmp_gt_i32_e64 s[40:41], 2, v121
	s_and_b64 s[42:43], s[44:45], s[42:43]
	v_cmp_gt_i32_e64 s[38:39], 1, v121
	s_and_b64 s[40:41], s[42:43], s[40:41]
	v_cmp_gt_i32_e64 s[36:37], 0, v121
	s_and_b64 s[38:39], s[40:41], s[38:39]
	s_and_b64 s[36:37], s[38:39], s[36:37]
	v_cmp_gt_i32_e64 s[34:35], 58, v121
	v_cndmask_b32_e64 v66, v66, v160, s[36:37]
	v_cmp_gt_i32_e64 s[36:37], 59, v121
	v_cmp_gt_i32_e64 s[30:31], 57, v121
	s_and_b64 s[34:35], s[36:37], s[34:35]
	v_cmp_gt_i32_e64 s[28:29], 56, v121
	s_and_b64 s[30:31], s[34:35], s[30:31]
	v_cmp_gt_i32_e64 s[26:27], 51, v121
	s_and_b64 s[28:29], s[30:31], s[28:29]
	v_cmp_gt_i32_e64 s[24:25], 50, v121
	s_and_b64 s[26:27], s[28:29], s[26:27]
	v_cmp_gt_i32_e64 s[22:23], 49, v121
	s_and_b64 s[24:25], s[26:27], s[24:25]
	v_cmp_gt_i32_e64 s[20:21], 48, v121
	s_and_b64 s[22:23], s[24:25], s[22:23]
	v_cmp_gt_i32_e64 s[18:19], 43, v121
	s_and_b64 s[20:21], s[22:23], s[20:21]
	v_cmp_gt_i32_e64 s[16:17], 42, v121
	s_and_b64 s[18:19], s[20:21], s[18:19]
	v_cmp_gt_i32_e64 s[14:15], 41, v121
	s_and_b64 s[16:17], s[18:19], s[16:17]
	v_cmp_gt_i32_e64 s[12:13], 40, v121
	s_and_b64 s[14:15], s[16:17], s[14:15]
	v_cmp_gt_i32_e64 s[10:11], 35, v121
	s_and_b64 s[12:13], s[14:15], s[12:13]
	v_cmp_gt_i32_e64 s[8:9], 34, v121
	s_and_b64 s[10:11], s[12:13], s[10:11]
	v_cmp_gt_i32_e64 s[6:7], 33, v121
	s_and_b64 s[8:9], s[10:11], s[8:9]
	v_cmp_gt_i32_e32 vcc, 32, v121
	s_and_b64 s[6:7], s[8:9], s[6:7]
	s_and_b64 vcc, s[6:7], vcc
	v_cndmask_b32_e64 v81, v81, v160, s[68:69]
	v_cndmask_b32_e64 v80, v80, v160, s[66:67]
	v_cndmask_b32_e64 v79, v79, v160, s[64:65]
	v_cndmask_b32_e64 v78, v78, v160, s[62:63]
	v_cndmask_b32_e64 v77, v77, v160, s[60:61]
	v_cndmask_b32_e64 v76, v76, v160, s[58:59]
	v_cndmask_b32_e64 v75, v75, v160, s[56:57]
	v_cndmask_b32_e64 v74, v74, v160, s[54:55]
	v_cndmask_b32_e64 v73, v73, v160, s[52:53]
	v_cndmask_b32_e64 v72, v72, v160, s[50:51]
	v_cndmask_b32_e64 v71, v71, v160, s[48:49]
	v_cndmask_b32_e64 v70, v70, v160, s[44:45]
	v_cndmask_b32_e64 v69, v69, v160, s[42:43]
	v_cndmask_b32_e64 v68, v68, v160, s[40:41]
	v_cndmask_b32_e64 v67, v67, v160, s[38:39]
	v_cndmask_b32_e64 v97, v97, v160, s[36:37]
	v_cndmask_b32_e64 v96, v96, v160, s[34:35]
	v_cndmask_b32_e64 v95, v95, v160, s[30:31]
	v_cndmask_b32_e64 v94, v94, v160, s[28:29]
	v_cndmask_b32_e64 v93, v93, v160, s[26:27]
	v_cndmask_b32_e64 v92, v92, v160, s[24:25]
	v_cndmask_b32_e64 v91, v91, v160, s[22:23]
	v_cndmask_b32_e64 v90, v90, v160, s[20:21]
	v_cndmask_b32_e64 v89, v89, v160, s[18:19]
	v_cndmask_b32_e64 v88, v88, v160, s[16:17]
	v_cndmask_b32_e64 v87, v87, v160, s[14:15]
	v_cndmask_b32_e64 v86, v86, v160, s[12:13]
	v_cndmask_b32_e64 v85, v85, v160, s[10:11]
	v_cndmask_b32_e64 v84, v84, v160, s[8:9]
	v_cndmask_b32_e64 v83, v83, v160, s[6:7]
	v_cndmask_b32_e32 v82, v82, v160, vcc

.LBB0_263:
	v_cndmask_b32_e64 v122, v121, v120, s[6:7]
	s_waitcnt vmcnt(0)
	v_mul_f32_e32 v120, 0xbe38aa3b, v122
	v_pk_fma_f32 v[80:81], v[80:81], s[84:85], v[120:121] op_sel_hi:[1,0,0]
	v_pk_fma_f32 v[78:79], v[78:79], s[84:85], v[120:121] op_sel_hi:[1,0,0]
	v_pk_fma_f32 v[76:77], v[76:77], s[84:85], v[120:121] op_sel_hi:[1,0,0]
	v_pk_fma_f32 v[74:75], v[74:75], s[84:85], v[120:121] op_sel_hi:[1,0,0]
	v_pk_fma_f32 v[72:73], v[72:73], s[84:85], v[120:121] op_sel_hi:[1,0,0]
	v_pk_fma_f32 v[70:71], v[70:71], s[84:85], v[120:121] op_sel_hi:[1,0,0]
	v_pk_fma_f32 v[68:69], v[68:69], s[84:85], v[120:121] op_sel_hi:[1,0,0]
	v_pk_fma_f32 v[66:67], v[66:67], s[84:85], v[120:121] op_sel_hi:[1,0,0]
	v_pk_fma_f32 v[186:187], v[88:89], s[84:85], v[120:121] op_sel_hi:[1,0,0]
	v_pk_fma_f32 v[196:197], v[86:87], s[84:85], v[120:121] op_sel_hi:[1,0,0]
	v_pk_fma_f32 v[86:87], v[84:85], s[84:85], v[120:121] op_sel_hi:[1,0,0]
	v_pk_fma_f32 v[88:89], v[82:83], s[84:85], v[120:121] op_sel_hi:[1,0,0]
	v_pk_fma_f32 v[148:149], v[96:97], s[84:85], v[120:121] op_sel_hi:[1,0,0]
	v_pk_fma_f32 v[150:151], v[94:95], s[84:85], v[120:121] op_sel_hi:[1,0,0]
	v_pk_fma_f32 v[152:153], v[92:93], s[84:85], v[120:121] op_sel_hi:[1,0,0]
	v_pk_fma_f32 v[154:155], v[90:91], s[84:85], v[120:121] op_sel_hi:[1,0,0]
	v_exp_f32_e32 v198, v66
	v_exp_f32_e32 v199, v67
	v_exp_f32_e32 v200, v68
	v_exp_f32_e32 v201, v69
	v_exp_f32_e32 v202, v70
	v_exp_f32_e32 v203, v71
	v_exp_f32_e32 v204, v72
	v_exp_f32_e32 v205, v73
	v_exp_f32_e32 v206, v74
	v_exp_f32_e32 v207, v75
	v_exp_f32_e32 v208, v76
	v_exp_f32_e32 v209, v77
	v_exp_f32_e32 v210, v78
	v_exp_f32_e32 v211, v79
	v_exp_f32_e32 v212, v80
	v_exp_f32_e32 v213, v81
	s_barrier
	s_add_u32 s6, s72, 0x180000
	s_addc_u32 s7, s73, 0
	s_mov_b32 m0, s85
	s_nop 0
	global_load_lds_dwordx4 v168, s[6:7] offset:0
	s_add_u32 s6, s88, 0x180000
	s_addc_u32 s7, s89, 0
	s_mov_b32 m0, s82
	s_nop 0
	global_load_lds_dwordx4 v169, s[6:7] offset:0
	s_nop 0
	s_mov_b32 m0, s83
	s_nop 0
	global_load_lds_dwordx4 v170, s[6:7] offset:0
	ds_read_b128 v[66:69], v175
	ds_read_b128 v[82:85], v175 offset:4096
	ds_read_b128 v[124:127], v176
	ds_read_b128 v[128:131], v176 offset:4096
	v_exp_f32_e32 v214, v88
	s_waitcnt lgkmcnt(3)
	v_mfma_f32_32x32x16_bf16 v[66:81], v[66:69], v[110:113], 0
	v_exp_f32_e32 v215, v89
	v_exp_f32_e32 v216, v86
	v_exp_f32_e32 v217, v87
	ds_read_b128 v[132:135], v177
	ds_read_b128 v[136:139], v177 offset:4096
	ds_read_b128 v[140:143], v178
	ds_read_b128 v[144:147], v178 offset:4096
	v_exp_f32_e32 v196, v196
	v_exp_f32_e32 v197, v197
	v_exp_f32_e32 v218, v186
	s_waitcnt lgkmcnt(6)
	v_mfma_f32_32x32x16_bf16 v[82:97], v[82:85], v[110:113], 0
	v_exp_f32_e32 v219, v187
	v_exp_f32_e32 v154, v154
	v_exp_f32_e32 v155, v155
	v_exp_f32_e32 v152, v152
	v_exp_f32_e32 v153, v153
	v_exp_f32_e32 v150, v150
	v_exp_f32_e32 v151, v151
	s_waitcnt lgkmcnt(5)
	v_mfma_f32_32x32x16_bf16 v[66:81], v[124:127], v[106:109], v[66:81]
	v_exp_f32_e32 v148, v148
	v_exp_f32_e32 v149, v149
	v_pk_add_f32 v[120:121], v[208:209], v[152:153]
	v_pk_add_f32 v[124:125], v[200:201], v[216:217]
	v_pk_add_f32 v[186:187], v[198:199], v[214:215]
	v_pk_add_f32 v[126:127], v[212:213], v[148:149]
	v_pk_add_f32 v[220:221], v[210:211], v[150:151]
	s_waitcnt lgkmcnt(4)
	v_mfma_f32_32x32x16_bf16 v[82:97], v[128:131], v[106:109], v[82:97]
	v_pk_add_f32 v[128:129], v[204:205], v[218:219]
	v_pk_add_f32 v[130:131], v[206:207], v[154:155]
	v_pk_add_f32 v[222:223], v[202:203], v[196:197]
	v_pk_add_f32 v[130:131], v[186:187], v[130:131]
	v_pk_add_f32 v[220:221], v[222:223], v[220:221]
	v_pk_add_f32 v[126:127], v[128:129], v[126:127]
	v_pk_add_f32 v[120:121], v[124:125], v[120:121]
	s_waitcnt lgkmcnt(3)
	v_mfma_f32_32x32x16_bf16 v[66:81], v[132:135], v[102:105], v[66:81]
	v_pk_add_f32 v[120:121], v[120:121], v[126:127]
	v_pk_add_f32 v[124:125], v[130:131], v[220:221]
	v_pk_add_f32 v[120:121], v[124:125], v[120:121]
	v_cvt_pk_bf16_f32 v124, v198, v199
	v_cvt_pk_bf16_f32 v125, v200, v201
	v_cvt_pk_bf16_f32 v126, v202, v203
	s_waitcnt lgkmcnt(2)
	v_mfma_f32_32x32x16_bf16 v[82:97], v[136:139], v[102:105], v[82:97]
	v_pk_add_f32 v[120:121], v[120:121], v[120:121] op_sel:[0,1] op_sel_hi:[1,0]
	v_cvt_pk_bf16_f32 v127, v204, v205
	v_cvt_pk_bf16_f32 v128, v206, v207
	v_cvt_pk_bf16_f32 v129, v208, v209
	v_cvt_pk_bf16_f32 v130, v210, v211
	v_cvt_pk_bf16_f32 v131, v212, v213
	s_nop 0
	v_mov_b32_e32 v186, v120
	s_waitcnt lgkmcnt(1)
	v_mfma_f32_32x32x16_bf16 v[66:81], v[140:143], v[98:101], v[66:81]
	v_permlane32_swap_b32_e32 v120, v186
	v_cvt_pk_bf16_f32 v132, v214, v215
	v_cvt_pk_bf16_f32 v133, v216, v217
	v_cvt_pk_bf16_f32 v134, v196, v197
	v_cvt_pk_bf16_f32 v135, v218, v219
	v_cvt_pk_bf16_f32 v136, v154, v155
	s_waitcnt lgkmcnt(0)
	v_mfma_f32_32x32x16_bf16 v[82:97], v[144:147], v[98:101], v[82:97]
	v_cvt_pk_bf16_f32 v137, v152, v153
	v_cvt_pk_bf16_f32 v138, v150, v151
	v_cvt_pk_bf16_f32 v139, v148, v149
	v_permlane32_swap_b32_e32 v124, v126
	v_permlane32_swap_b32_e32 v125, v127
	v_permlane32_swap_b32_e32 v128, v130
	v_permlane32_swap_b32_e32 v129, v131
	v_permlane32_swap_b32_e32 v132, v134
	v_permlane32_swap_b32_e32 v133, v135
	v_permlane32_swap_b32_e32 v136, v138
	v_permlane32_swap_b32_e32 v137, v139
	ds_read_b64_tr_b16 v[140:141], v166 offset:0
	ds_read_b64_tr_b16 v[142:143], v166 offset:0x800
	ds_read_b64_tr_b16 v[144:145], v166 offset:0x1000
	ds_read_b64_tr_b16 v[146:147], v166 offset:0x1800
	ds_read_b64_tr_b16 v[148:149], v166 offset:0x2000
	ds_read_b64_tr_b16 v[150:151], v166 offset:0x2800
	ds_read_b64_tr_b16 v[152:153], v166 offset:0x3000
	ds_read_b64_tr_b16 v[154:155], v166 offset:0x3800
	ds_read_b64_tr_b16 v[196:197], v166 offset:0x200
	ds_read_b64_tr_b16 v[198:199], v166 offset:0xa00
	ds_read_b64_tr_b16 v[200:201], v166 offset:0x1200
	ds_read_b64_tr_b16 v[202:203], v166 offset:0x1a00
	ds_read_b64_tr_b16 v[204:205], v166 offset:0x2200
	ds_read_b64_tr_b16 v[206:207], v166 offset:0x2a00
	ds_read_b64_tr_b16 v[208:209], v166 offset:0x3200
	ds_read_b64_tr_b16 v[210:211], v166 offset:0x3a00
	s_waitcnt lgkmcnt(8)
	s_nop 0
	v_mfma_f32_32x32x16_bf16 v[18:33], v[124:127], v[140:143], v[18:33]
	v_mfma_f32_32x32x16_bf16 v[18:33], v[128:131], v[144:147], v[18:33]
	v_mfma_f32_32x32x16_bf16 v[18:33], v[132:135], v[148:151], v[18:33]
	v_mfma_f32_32x32x16_bf16 v[18:33], v[136:139], v[152:155], v[18:33]
	ds_read_b64_tr_b16 v[140:141], v166 offset:0x400
	ds_read_b64_tr_b16 v[142:143], v166 offset:0xc00
	ds_read_b64_tr_b16 v[144:145], v166 offset:0x1400
	ds_read_b64_tr_b16 v[146:147], v166 offset:0x1c00
	ds_read_b64_tr_b16 v[148:149], v166 offset:0x2400
	ds_read_b64_tr_b16 v[150:151], v166 offset:0x2c00
	ds_read_b64_tr_b16 v[152:153], v166 offset:0x3400
	ds_read_b64_tr_b16 v[154:155], v166 offset:0x3c00
	s_waitcnt lgkmcnt(8)
	v_mfma_f32_32x32x16_bf16 v[34:49], v[124:127], v[196:199], v[34:49]
	v_mfma_f32_32x32x16_bf16 v[34:49], v[128:131], v[200:203], v[34:49]
	v_mfma_f32_32x32x16_bf16 v[34:49], v[132:135], v[204:207], v[34:49]
	v_mfma_f32_32x32x16_bf16 v[34:49], v[136:139], v[208:211], v[34:49]
	ds_read_b64_tr_b16 v[196:197], v166 offset:0x600
	ds_read_b64_tr_b16 v[198:199], v166 offset:0xe00
	ds_read_b64_tr_b16 v[200:201], v166 offset:0x1600
	ds_read_b64_tr_b16 v[202:203], v166 offset:0x1e00
	ds_read_b64_tr_b16 v[204:205], v166 offset:0x2600
	ds_read_b64_tr_b16 v[206:207], v166 offset:0x2e00
	ds_read_b64_tr_b16 v[208:209], v166 offset:0x3600
	ds_read_b64_tr_b16 v[210:211], v166 offset:0x3e00
	s_waitcnt lgkmcnt(8)
	v_mfma_f32_32x32x16_bf16 v[50:65], v[124:127], v[140:143], v[50:65]
	v_mfma_f32_32x32x16_bf16 v[50:65], v[128:131], v[144:147], v[50:65]
	v_mfma_f32_32x32x16_bf16 v[50:65], v[132:135], v[148:151], v[50:65]
	v_mfma_f32_32x32x16_bf16 v[50:65], v[136:139], v[152:155], v[50:65]
	s_waitcnt lgkmcnt(0)
	v_mfma_f32_32x32x16_bf16 v[2:17], v[124:127], v[196:199], v[2:17]
	s_sub_i32 s6, s95, 64
	s_cmp_le_i32 s6, s77
	v_mfma_f32_32x32x16_bf16 v[2:17], v[128:131], v[200:203], v[2:17]
	v_mfma_f32_32x32x16_bf16 v[2:17], v[132:135], v[204:207], v[2:17]
	v_mfma_f32_32x32x16_bf16 v[2:17], v[136:139], v[208:211], v[2:17]
	s_cbranch_scc1 .LBB0_265
	v_add_u32_e32 v121, 0xffffff80, v183
	v_cmp_gt_i32_e64 s[66:67], 26, v121
	v_cmp_gt_i32_e64 s[68:69], 27, v121
	v_cmp_gt_i32_e64 s[64:65], 25, v121
	s_and_b64 s[66:67], s[68:69], s[66:67]
	v_cmp_gt_i32_e64 s[62:63], 24, v121
	s_and_b64 s[64:65], s[66:67], s[64:65]
	v_cmp_gt_i32_e64 s[60:61], 19, v121
	s_and_b64 s[62:63], s[64:65], s[62:63]
	v_cmp_gt_i32_e64 s[58:59], 18, v121
	s_and_b64 s[60:61], s[62:63], s[60:61]
	v_cmp_gt_i32_e64 s[56:57], 17, v121
	s_and_b64 s[58:59], s[60:61], s[58:59]
	v_cmp_gt_i32_e64 s[54:55], 16, v121
	s_and_b64 s[56:57], s[58:59], s[56:57]
	v_cmp_gt_i32_e64 s[52:53], 11, v121
	s_and_b64 s[54:55], s[56:57], s[54:55]
	v_cmp_gt_i32_e64 s[50:51], 10, v121
	s_and_b64 s[52:53], s[54:55], s[52:53]
	v_cmp_gt_i32_e64 s[48:49], 9, v121
	s_and_b64 s[50:51], s[52:53], s[50:51]
	v_cmp_gt_i32_e64 s[44:45], 8, v121
	s_and_b64 s[48:49], s[50:51], s[48:49]
	v_cmp_gt_i32_e64 s[42:43], 3, v121
	s_and_b64 s[44:45], s[48:49], s[44:45]
	v_cmp_gt_i32_e64 s[40:41], 2, v121
	s_and_b64 s[42:43], s[44:45], s[42:43]
	v_cmp_gt_i32_e64 s[38:39], 1, v121
	s_and_b64 s[40:41], s[42:43], s[40:41]
	v_cmp_gt_i32_e64 s[36:37], 0, v121
	s_and_b64 s[38:39], s[40:41], s[38:39]
	s_and_b64 s[36:37], s[38:39], s[36:37]
	v_cmp_gt_i32_e64 s[34:35], 58, v121
	v_cndmask_b32_e64 v66, v66, v160, s[36:37]
	v_cmp_gt_i32_e64 s[36:37], 59, v121
	v_cmp_gt_i32_e64 s[30:31], 57, v121
	s_and_b64 s[34:35], s[36:37], s[34:35]
	v_cmp_gt_i32_e64 s[28:29], 56, v121
	s_and_b64 s[30:31], s[34:35], s[30:31]
	v_cmp_gt_i32_e64 s[26:27], 51, v121
	s_and_b64 s[28:29], s[30:31], s[28:29]
	v_cmp_gt_i32_e64 s[24:25], 50, v121
	s_and_b64 s[26:27], s[28:29], s[26:27]
	v_cmp_gt_i32_e64 s[22:23], 49, v121
	s_and_b64 s[24:25], s[26:27], s[24:25]
	v_cmp_gt_i32_e64 s[20:21], 48, v121
	s_and_b64 s[22:23], s[24:25], s[22:23]
	v_cmp_gt_i32_e64 s[18:19], 43, v121
	s_and_b64 s[20:21], s[22:23], s[20:21]
	v_cmp_gt_i32_e64 s[16:17], 42, v121
	s_and_b64 s[18:19], s[20:21], s[18:19]
	v_cmp_gt_i32_e64 s[14:15], 41, v121
	s_and_b64 s[16:17], s[18:19], s[16:17]
	v_cmp_gt_i32_e64 s[12:13], 40, v121
	s_and_b64 s[14:15], s[16:17], s[14:15]
	v_cmp_gt_i32_e64 s[10:11], 35, v121
	s_and_b64 s[12:13], s[14:15], s[12:13]
	v_cmp_gt_i32_e64 s[8:9], 34, v121
	s_and_b64 s[10:11], s[12:13], s[10:11]
	v_cmp_gt_i32_e64 s[6:7], 33, v121
	s_and_b64 s[8:9], s[10:11], s[8:9]
	v_cmp_gt_i32_e32 vcc, 32, v121
	s_and_b64 s[6:7], s[8:9], s[6:7]
	s_and_b64 vcc, s[6:7], vcc
	v_cndmask_b32_e64 v81, v81, v160, s[68:69]
	v_cndmask_b32_e64 v80, v80, v160, s[66:67]
	v_cndmask_b32_e64 v79, v79, v160, s[64:65]
	v_cndmask_b32_e64 v78, v78, v160, s[62:63]
	v_cndmask_b32_e64 v77, v77, v160, s[60:61]
	v_cndmask_b32_e64 v76, v76, v160, s[58:59]
	v_cndmask_b32_e64 v75, v75, v160, s[56:57]
	v_cndmask_b32_e64 v74, v74, v160, s[54:55]
	v_cndmask_b32_e64 v73, v73, v160, s[52:53]
	v_cndmask_b32_e64 v72, v72, v160, s[50:51]
	v_cndmask_b32_e64 v71, v71, v160, s[48:49]
	v_cndmask_b32_e64 v70, v70, v160, s[44:45]
	v_cndmask_b32_e64 v69, v69, v160, s[42:43]
	v_cndmask_b32_e64 v68, v68, v160, s[40:41]
	v_cndmask_b32_e64 v67, v67, v160, s[38:39]
	v_cndmask_b32_e64 v97, v97, v160, s[36:37]
	v_cndmask_b32_e64 v96, v96, v160, s[34:35]
	v_cndmask_b32_e64 v95, v95, v160, s[30:31]
	v_cndmask_b32_e64 v94, v94, v160, s[28:29]
	v_cndmask_b32_e64 v93, v93, v160, s[26:27]
	v_cndmask_b32_e64 v92, v92, v160, s[24:25]
	v_cndmask_b32_e64 v91, v91, v160, s[22:23]
	v_cndmask_b32_e64 v90, v90, v160, s[20:21]
	v_cndmask_b32_e64 v89, v89, v160, s[18:19]
	v_cndmask_b32_e64 v88, v88, v160, s[16:17]
	v_cndmask_b32_e64 v87, v87, v160, s[14:15]
	v_cndmask_b32_e64 v86, v86, v160, s[12:13]
	v_cndmask_b32_e64 v85, v85, v160, s[10:11]
	v_cndmask_b32_e64 v84, v84, v160, s[8:9]
	v_cndmask_b32_e64 v83, v83, v160, s[6:7]
	v_cndmask_b32_e32 v82, v82, v160, vcc

.LBB0_269:
	v_cndmask_b32_e64 v121, v121, v122, s[6:7]
	s_waitcnt vmcnt(0)
	v_mul_f32_e32 v122, 0xbe38aa3b, v121
	v_pk_fma_f32 v[80:81], v[80:81], s[84:85], v[122:123] op_sel_hi:[1,0,0]
	v_pk_fma_f32 v[78:79], v[78:79], s[84:85], v[122:123] op_sel_hi:[1,0,0]
	v_pk_fma_f32 v[76:77], v[76:77], s[84:85], v[122:123] op_sel_hi:[1,0,0]
	v_pk_fma_f32 v[74:75], v[74:75], s[84:85], v[122:123] op_sel_hi:[1,0,0]
	v_pk_fma_f32 v[72:73], v[72:73], s[84:85], v[122:123] op_sel_hi:[1,0,0]
	v_pk_fma_f32 v[70:71], v[70:71], s[84:85], v[122:123] op_sel_hi:[1,0,0]
	v_pk_fma_f32 v[68:69], v[68:69], s[84:85], v[122:123] op_sel_hi:[1,0,0]
	v_pk_fma_f32 v[66:67], v[66:67], s[84:85], v[122:123] op_sel_hi:[1,0,0]
	v_pk_fma_f32 v[138:139], v[96:97], s[84:85], v[122:123] op_sel_hi:[1,0,0]
	v_pk_fma_f32 v[148:149], v[94:95], s[84:85], v[122:123] op_sel_hi:[1,0,0]
	v_pk_fma_f32 v[150:151], v[92:93], s[84:85], v[122:123] op_sel_hi:[1,0,0]
	v_pk_fma_f32 v[152:153], v[90:91], s[84:85], v[122:123] op_sel_hi:[1,0,0]
	v_pk_fma_f32 v[154:155], v[88:89], s[84:85], v[122:123] op_sel_hi:[1,0,0]
	v_pk_fma_f32 v[196:197], v[86:87], s[84:85], v[122:123] op_sel_hi:[1,0,0]
	v_pk_fma_f32 v[198:199], v[84:85], s[84:85], v[122:123] op_sel_hi:[1,0,0]
	v_pk_fma_f32 v[200:201], v[82:83], s[84:85], v[122:123] op_sel_hi:[1,0,0]
	v_exp_f32_e32 v202, v66
	v_exp_f32_e32 v203, v67
	v_exp_f32_e32 v204, v68
	v_exp_f32_e32 v205, v69
	v_exp_f32_e32 v206, v70
	v_exp_f32_e32 v207, v71
	v_exp_f32_e32 v208, v72
	v_exp_f32_e32 v209, v73
	v_exp_f32_e32 v210, v74
	v_exp_f32_e32 v211, v75
	v_exp_f32_e32 v212, v76
	v_exp_f32_e32 v213, v77
	v_exp_f32_e32 v214, v78
	v_exp_f32_e32 v215, v79
	v_exp_f32_e32 v216, v80
	v_exp_f32_e32 v217, v81
	s_barrier
	s_add_u32 s6, s72, 0x1c0000
	s_addc_u32 s7, s73, 0
	s_mov_b32 m0, s81
	s_nop 0
	global_load_lds_dwordx4 v168, s[6:7] offset:0
	s_add_u32 s6, s88, 0x1c0000
	s_addc_u32 s7, s89, 0
	s_mov_b32 m0, s78
	s_nop 0
	global_load_lds_dwordx4 v169, s[6:7] offset:0
	s_nop 0
	s_mov_b32 m0, s79
	s_nop 0
	global_load_lds_dwordx4 v170, s[6:7] offset:0
	ds_read_b128 v[66:69], v171
	ds_read_b128 v[70:73], v171 offset:4096
	ds_read_b128 v[122:125], v172
	ds_read_b128 v[126:129], v172 offset:4096
	ds_read_b128 v[130:133], v173
	ds_read_b128 v[134:137], v173 offset:4096
	ds_read_b128 v[140:143], v174
	ds_read_b128 v[144:147], v174 offset:4096
	s_waitcnt lgkmcnt(7)
	v_mfma_f32_32x32x16_bf16 v[82:97], v[66:69], v[110:113], 0
	v_exp_f32_e32 v200, v200
	v_exp_f32_e32 v201, v201
	v_exp_f32_e32 v198, v198
	v_exp_f32_e32 v199, v199
	v_exp_f32_e32 v196, v196
	v_exp_f32_e32 v197, v197
	v_exp_f32_e32 v154, v154
	s_waitcnt lgkmcnt(6)
	v_mfma_f32_32x32x16_bf16 v[66:81], v[70:73], v[110:113], 0
	v_exp_f32_e32 v155, v155
	v_exp_f32_e32 v152, v152
	v_exp_f32_e32 v153, v153
	v_exp_f32_e32 v150, v150
	v_exp_f32_e32 v151, v151
	v_exp_f32_e32 v148, v148
	v_exp_f32_e32 v149, v149
	s_waitcnt lgkmcnt(5)
	v_mfma_f32_32x32x16_bf16 v[82:97], v[122:125], v[106:109], v[82:97]
	v_exp_f32_e32 v218, v138
	v_exp_f32_e32 v219, v139
	v_pk_add_f32 v[122:123], v[212:213], v[150:151]
	v_pk_add_f32 v[124:125], v[204:205], v[198:199]
	v_pk_add_f32 v[138:139], v[210:211], v[152:153]
	v_pk_add_f32 v[220:221], v[202:203], v[200:201]
	v_pk_add_f32 v[222:223], v[214:215], v[148:149]
	s_waitcnt lgkmcnt(4)
	v_mfma_f32_32x32x16_bf16 v[66:81], v[126:129], v[106:109], v[66:81]
	v_pk_add_f32 v[126:127], v[216:217], v[218:219]
	v_pk_add_f32 v[128:129], v[208:209], v[154:155]
	v_pk_add_f32 v[224:225], v[206:207], v[196:197]
	v_pk_add_f32 v[126:127], v[128:129], v[126:127]
	v_pk_add_f32 v[222:223], v[224:225], v[222:223]
	v_pk_add_f32 v[122:123], v[124:125], v[122:123]
	s_waitcnt lgkmcnt(3)
	v_mfma_f32_32x32x16_bf16 v[82:97], v[130:133], v[102:105], v[82:97]
	v_pk_add_f32 v[130:131], v[220:221], v[138:139]
	v_pk_add_f32 v[122:123], v[122:123], v[126:127]
	v_pk_add_f32 v[124:125], v[130:131], v[222:223]
	v_pk_add_f32 v[122:123], v[124:125], v[122:123]
	s_nop 0
	v_pk_add_f32 v[138:139], v[122:123], v[122:123] op_sel:[0,1] op_sel_hi:[1,0]
	s_waitcnt lgkmcnt(2)
	v_mfma_f32_32x32x16_bf16 v[66:81], v[134:137], v[102:105], v[66:81]
	v_mov_b32_e32 v195, v138
	s_nop 1
	v_permlane32_swap_b32_e32 v138, v195
	v_cvt_pk_bf16_f32 v122, v202, v203
	v_cvt_pk_bf16_f32 v123, v204, v205
	v_cvt_pk_bf16_f32 v124, v206, v207
	v_cvt_pk_bf16_f32 v125, v208, v209
	s_waitcnt lgkmcnt(1)
	v_mfma_f32_32x32x16_bf16 v[82:97], v[140:143], v[98:101], v[82:97]
	v_cvt_pk_bf16_f32 v126, v210, v211
	v_cvt_pk_bf16_f32 v127, v212, v213
	v_cvt_pk_bf16_f32 v128, v214, v215
	v_cvt_pk_bf16_f32 v129, v216, v217
	v_cvt_pk_bf16_f32 v130, v200, v201
	v_cvt_pk_bf16_f32 v131, v198, v199
	v_cvt_pk_bf16_f32 v132, v196, v197
	s_waitcnt lgkmcnt(0)
	v_mfma_f32_32x32x16_bf16 v[66:81], v[144:147], v[98:101], v[66:81]
	v_cvt_pk_bf16_f32 v133, v154, v155
	v_cvt_pk_bf16_f32 v134, v152, v153
	v_cvt_pk_bf16_f32 v135, v150, v151
	v_cvt_pk_bf16_f32 v136, v148, v149
	v_cvt_pk_bf16_f32 v137, v218, v219
	v_permlane32_swap_b32_e32 v122, v124
	v_permlane32_swap_b32_e32 v123, v125
	v_permlane32_swap_b32_e32 v126, v128
	v_permlane32_swap_b32_e32 v127, v129
	v_permlane32_swap_b32_e32 v130, v132
	v_permlane32_swap_b32_e32 v131, v133
	v_permlane32_swap_b32_e32 v134, v136
	v_permlane32_swap_b32_e32 v135, v137
	ds_read_b64_tr_b16 v[140:141], v166 offset:0x4000
	ds_read_b64_tr_b16 v[142:143], v166 offset:0x4800
	ds_read_b64_tr_b16 v[144:145], v166 offset:0x5000
	ds_read_b64_tr_b16 v[146:147], v166 offset:0x5800
	ds_read_b64_tr_b16 v[148:149], v166 offset:0x6000
	ds_read_b64_tr_b16 v[150:151], v166 offset:0x6800
	ds_read_b64_tr_b16 v[152:153], v166 offset:0x7000
	ds_read_b64_tr_b16 v[154:155], v166 offset:0x7800
	ds_read_b64_tr_b16 v[196:197], v166 offset:0x4200
	ds_read_b64_tr_b16 v[198:199], v166 offset:0x4a00
	ds_read_b64_tr_b16 v[200:201], v166 offset:0x5200
	ds_read_b64_tr_b16 v[202:203], v166 offset:0x5a00
	ds_read_b64_tr_b16 v[204:205], v166 offset:0x6200
	ds_read_b64_tr_b16 v[206:207], v166 offset:0x6a00
	ds_read_b64_tr_b16 v[208:209], v166 offset:0x7200
	ds_read_b64_tr_b16 v[210:211], v166 offset:0x7a00
	s_waitcnt lgkmcnt(8)
	s_nop 0
	v_mfma_f32_32x32x16_bf16 v[18:33], v[122:125], v[140:143], v[18:33]
	v_mfma_f32_32x32x16_bf16 v[18:33], v[126:129], v[144:147], v[18:33]
	v_mfma_f32_32x32x16_bf16 v[18:33], v[130:133], v[148:151], v[18:33]
	v_mfma_f32_32x32x16_bf16 v[18:33], v[134:137], v[152:155], v[18:33]
	ds_read_b64_tr_b16 v[140:141], v166 offset:0x4400
	ds_read_b64_tr_b16 v[142:143], v166 offset:0x4c00
	ds_read_b64_tr_b16 v[144:145], v166 offset:0x5400
	ds_read_b64_tr_b16 v[146:147], v166 offset:0x5c00
	ds_read_b64_tr_b16 v[148:149], v166 offset:0x6400
	ds_read_b64_tr_b16 v[150:151], v166 offset:0x6c00
	ds_read_b64_tr_b16 v[152:153], v166 offset:0x7400
	ds_read_b64_tr_b16 v[154:155], v166 offset:0x7c00
	s_waitcnt lgkmcnt(8)
	v_mfma_f32_32x32x16_bf16 v[34:49], v[122:125], v[196:199], v[34:49]
	v_mfma_f32_32x32x16_bf16 v[34:49], v[126:129], v[200:203], v[34:49]
	v_mfma_f32_32x32x16_bf16 v[34:49], v[130:133], v[204:207], v[34:49]
	v_mfma_f32_32x32x16_bf16 v[34:49], v[134:137], v[208:211], v[34:49]
	ds_read_b64_tr_b16 v[196:197], v166 offset:0x4600
	ds_read_b64_tr_b16 v[198:199], v166 offset:0x4e00
	ds_read_b64_tr_b16 v[200:201], v166 offset:0x5600
	ds_read_b64_tr_b16 v[202:203], v166 offset:0x5e00
	ds_read_b64_tr_b16 v[204:205], v166 offset:0x6600
	ds_read_b64_tr_b16 v[206:207], v166 offset:0x6e00
	ds_read_b64_tr_b16 v[208:209], v166 offset:0x7600
	ds_read_b64_tr_b16 v[210:211], v166 offset:0x7e00
	s_waitcnt lgkmcnt(8)
	v_mfma_f32_32x32x16_bf16 v[50:65], v[122:125], v[140:143], v[50:65]
	v_mfma_f32_32x32x16_bf16 v[50:65], v[126:129], v[144:147], v[50:65]
	v_mfma_f32_32x32x16_bf16 v[50:65], v[130:133], v[148:151], v[50:65]
	v_mfma_f32_32x32x16_bf16 v[50:65], v[134:137], v[152:155], v[50:65]
	s_waitcnt lgkmcnt(0)
	v_mfma_f32_32x32x16_bf16 v[2:17], v[122:125], v[196:199], v[2:17]
	s_cmp_le_i32 s95, s77
	v_mfma_f32_32x32x16_bf16 v[2:17], v[126:129], v[200:203], v[2:17]
	v_mfma_f32_32x32x16_bf16 v[2:17], v[130:133], v[204:207], v[2:17]
	v_mfma_f32_32x32x16_bf16 v[2:17], v[134:137], v[208:211], v[2:17]
	s_cbranch_scc1 .LBB0_271
	v_add_u32_e32 v122, 0xffffff40, v183
	v_cmp_gt_i32_e64 s[66:67], 26, v122
	v_cmp_gt_i32_e64 s[68:69], 27, v122
	v_cmp_gt_i32_e64 s[64:65], 25, v122
	s_and_b64 s[66:67], s[68:69], s[66:67]
	v_cmp_gt_i32_e64 s[62:63], 24, v122
	s_and_b64 s[64:65], s[66:67], s[64:65]
	v_cmp_gt_i32_e64 s[60:61], 19, v122
	s_and_b64 s[62:63], s[64:65], s[62:63]
	v_cmp_gt_i32_e64 s[58:59], 18, v122
	s_and_b64 s[60:61], s[62:63], s[60:61]
	v_cmp_gt_i32_e64 s[56:57], 17, v122
	s_and_b64 s[58:59], s[60:61], s[58:59]
	v_cmp_gt_i32_e64 s[54:55], 16, v122
	s_and_b64 s[56:57], s[58:59], s[56:57]
	v_cmp_gt_i32_e64 s[52:53], 11, v122
	s_and_b64 s[54:55], s[56:57], s[54:55]
	v_cmp_gt_i32_e64 s[50:51], 10, v122
	s_and_b64 s[52:53], s[54:55], s[52:53]
	v_cmp_gt_i32_e64 s[48:49], 9, v122
	s_and_b64 s[50:51], s[52:53], s[50:51]
	v_cmp_gt_i32_e64 s[44:45], 8, v122
	s_and_b64 s[48:49], s[50:51], s[48:49]
	v_cmp_gt_i32_e64 s[42:43], 3, v122
	s_and_b64 s[44:45], s[48:49], s[44:45]
	v_cmp_gt_i32_e64 s[40:41], 2, v122
	s_and_b64 s[42:43], s[44:45], s[42:43]
	v_cmp_gt_i32_e64 s[38:39], 1, v122
	s_and_b64 s[40:41], s[42:43], s[40:41]
	v_cmp_gt_i32_e64 s[36:37], 0, v122
	s_and_b64 s[38:39], s[40:41], s[38:39]
	s_and_b64 s[36:37], s[38:39], s[36:37]
	v_cmp_gt_i32_e64 s[34:35], 58, v122
	v_cndmask_b32_e64 v82, v82, v160, s[36:37]
	v_cmp_gt_i32_e64 s[36:37], 59, v122
	v_cmp_gt_i32_e64 s[30:31], 57, v122
	s_and_b64 s[34:35], s[36:37], s[34:35]
	v_cmp_gt_i32_e64 s[28:29], 56, v122
	s_and_b64 s[30:31], s[34:35], s[30:31]
	v_cmp_gt_i32_e64 s[26:27], 51, v122
	s_and_b64 s[28:29], s[30:31], s[28:29]
	v_cmp_gt_i32_e64 s[24:25], 50, v122
	s_and_b64 s[26:27], s[28:29], s[26:27]
	v_cmp_gt_i32_e64 s[22:23], 49, v122
	s_and_b64 s[24:25], s[26:27], s[24:25]
	v_cmp_gt_i32_e64 s[20:21], 48, v122
	s_and_b64 s[22:23], s[24:25], s[22:23]
	v_cmp_gt_i32_e64 s[18:19], 43, v122
	s_and_b64 s[20:21], s[22:23], s[20:21]
	v_cmp_gt_i32_e64 s[16:17], 42, v122
	s_and_b64 s[18:19], s[20:21], s[18:19]
	v_cmp_gt_i32_e64 s[14:15], 41, v122
	s_and_b64 s[16:17], s[18:19], s[16:17]
	v_cmp_gt_i32_e64 s[12:13], 40, v122
	s_and_b64 s[14:15], s[16:17], s[14:15]
	v_cmp_gt_i32_e64 s[10:11], 35, v122
	s_and_b64 s[12:13], s[14:15], s[12:13]
	v_cmp_gt_i32_e64 s[8:9], 34, v122
	s_and_b64 s[10:11], s[12:13], s[10:11]
	v_cmp_gt_i32_e64 s[6:7], 33, v122
	s_and_b64 s[8:9], s[10:11], s[8:9]
	v_cmp_gt_i32_e32 vcc, 32, v122
	s_and_b64 s[6:7], s[8:9], s[6:7]
	s_and_b64 vcc, s[6:7], vcc
	v_cndmask_b32_e64 v97, v97, v160, s[68:69]
	v_cndmask_b32_e64 v96, v96, v160, s[66:67]
	v_cndmask_b32_e64 v95, v95, v160, s[64:65]
	v_cndmask_b32_e64 v94, v94, v160, s[62:63]
	v_cndmask_b32_e64 v93, v93, v160, s[60:61]
	v_cndmask_b32_e64 v92, v92, v160, s[58:59]
	v_cndmask_b32_e64 v91, v91, v160, s[56:57]
	v_cndmask_b32_e64 v90, v90, v160, s[54:55]
	v_cndmask_b32_e64 v89, v89, v160, s[52:53]
	v_cndmask_b32_e64 v88, v88, v160, s[50:51]
	v_cndmask_b32_e64 v87, v87, v160, s[48:49]
	v_cndmask_b32_e64 v86, v86, v160, s[44:45]
	v_cndmask_b32_e64 v85, v85, v160, s[42:43]
	v_cndmask_b32_e64 v84, v84, v160, s[40:41]
	v_cndmask_b32_e64 v83, v83, v160, s[38:39]
	v_cndmask_b32_e64 v81, v81, v160, s[36:37]
	v_cndmask_b32_e64 v80, v80, v160, s[34:35]
	v_cndmask_b32_e64 v79, v79, v160, s[30:31]
	v_cndmask_b32_e64 v78, v78, v160, s[28:29]
	v_cndmask_b32_e64 v77, v77, v160, s[26:27]
	v_cndmask_b32_e64 v76, v76, v160, s[24:25]
	v_cndmask_b32_e64 v75, v75, v160, s[22:23]
	v_cndmask_b32_e64 v74, v74, v160, s[20:21]
	v_cndmask_b32_e64 v73, v73, v160, s[18:19]
	v_cndmask_b32_e64 v72, v72, v160, s[16:17]
	v_cndmask_b32_e64 v71, v71, v160, s[14:15]
	v_cndmask_b32_e64 v70, v70, v160, s[12:13]
	v_cndmask_b32_e64 v69, v69, v160, s[10:11]
	v_cndmask_b32_e64 v68, v68, v160, s[8:9]
	v_cndmask_b32_e64 v67, v67, v160, s[6:7]
	v_cndmask_b32_e32 v66, v66, v160, vcc
